# post-norm-1 row loop (both layers): next-row prefetch into shadow VGPRs, hoisted input pointers, consumer vmcnt ladder removed
# speedup vs baseline: 1.0097x; 1.0097x over previous
; __device__ __forceinline__ void cvt8(const u32x4 r, float (&f)[8]) { f[0] = bflo(r.x); f[1] = bfhi(r.x); f[2] = bflo(r.y); f[3] = bfhi(r.y); f[4] = bflo(r.z); f[5] = bfhi(r.z); f[6] = bflo(r.w); f[7] = bfhi(r.w); }
; __device__ __forceinline__ void ph_post1(Ctx& C, int l, int nrows, bool dry = false) {
;     ...
;     int nit = 0, cur_mrow = -1;
;     const int nit_all = nrows / 8, it0 = (int)(((long)C.bid * nit_all) / C.G), it1 = (int)(((long)(C.bid + 1) * nit_all) / C.G);
;     for (int it = it0; it < it1; ++it, ++nit) {
;         const int row = it * 8 + C.wave;
;         const int mrow = row < NLAT ? row / SL : 4; const float* mod = WSP(float, WS_MOD) + (size_t)(l * 5 + mrow) * 12288;
;         __syncthreads();
;         if (mrow != cur_mrow) { stage2048(C, PAR, mod + 4096); stage2048(C, PAR + 2048, INP(I_LN1G) + l * DM); stage2048(C, PAR + 4096, INP(I_LN1B) + l * DM); stage2048(C, PAR + 6144, mod + 8192); stage2048(C, PAR + 8192, mod + 6144); cur_mrow = mrow; __syncthreads(); }
;         {
;             float v[32], y[32], g1[32];
;             if (l == 0) row_load(src_x0(C, row), C.lane, v); else row_load_bf16(WSP(bf16, WS_X) + (size_t)row * DM, C.lane, v);
;             row_load_lds(PAR, C.lane, g1);
;             { const bf16* yo = WSP(bf16, WS_YO) + (size_t)row * DM;
; #pragma unroll
;               for (int j = 0; j < 4; ++j) { float t8[8]; cvt8(*(const u32x4*)(yo + 512 * j + 8 * C.lane), t8);
; #pragma unroll
;                   for (int e = 0; e < 8; ++e) y[8 * j + e] = t8[e]; } }
.LBB0_1212:
	s_cmp_ge_i32 s22, s12
	s_mov_b32 s4, 0
	s_cbranch_scc1 .LBB0_1254
	v_and_b32_e32 v6, 63, v54
	v_mov_b32_e32 v57, 0
	v_lshlrev_b32_e32 v2, 4, v6
	v_mov_b32_e32 v3, v57
	v_lshl_add_u64 v[4:5], s[20:21], 0, v[2:3]
	s_mov_b64 s[4:5], 0x46900000
	v_lshlrev_b32_e32 v56, 3, v6
	v_lshl_add_u64 v[58:59], v[4:5], 0, s[4:5]
	s_mov_b64 s[4:5], 0x29400000
	s_ashr_i32 s3, s3, 6
	v_lshl_add_u64 v[60:61], v[4:5], 0, s[4:5]
	v_lshl_add_u64 v[4:5], s[20:21], 0, v[56:57]
	s_mov_b64 s[4:5], 0x4f100000
	v_lshl_add_u64 v[62:63], v[4:5], 0, s[4:5]
	s_lshl_b32 s4, s3, 13
	s_lshl_b32 s14, s3, 10
	s_add_i32 s15, 0, 0x10000
	s_add_i32 s18, s4, 0
	v_lshlrev_b32_e32 v4, 2, v54
	s_add_i32 s6, s15, s14
	v_add_u32_e32 v55, s6, v2
	s_add_u32 s19, s20, 0x100000
	v_and_b32_e32 v2, 0xffffff80, v4
	v_and_b32_e32 v7, 0x7c, v4
	v_and_b32_e32 v3, 0xe0, v4
	s_load_dwordx2 s[8:9], s[10:11], 0xf0
	s_addc_u32 s23, s21, 0
	v_add3_u32 v91, s15, v2, v7
	s_add_i32 s15, 0, 0x14000
	v_add3_u32 v92, s15, v2, v7
	v_lshl_or_b32 v2, s3, 8, v3
	v_ashrrev_i32_e32 v3, 31, v2
	v_lshlrev_b32_e32 v1, 5, v6
	v_cmp_gt_u32_e64 s[4:5], 8, v6
	s_add_i32 s24, 0, 0x16800
	v_lshlrev_b32_e32 v6, 4, v54
	v_lshlrev_b64 v[2:3], 7, v[2:3]
	v_and_b32_e32 v7, 7, v54
	v_add_u32_e32 v86, s24, v6
	s_add_i32 s24, 0, 0x18800
	v_lshl_or_b32 v2, v7, 4, v2
	v_add_u32_e32 v87, s24, v6
	s_add_i32 s24, 0, 0x1a800
	s_waitcnt lgkmcnt(0)
	v_lshl_add_u64 v[2:3], s[8:9], 0, v[2:3]
	s_mov_b64 s[8:9], 0x380
	v_add_u32_e32 v88, s24, v6
	s_add_i32 s24, 0, 0x1c800
	v_lshl_add_u64 v[64:65], v[2:3], 0, s[8:9]
	v_and_b32_e32 v2, 0x380, v6
	s_add_i32 s8, s14, 0
	s_movk_i32 s6, 0x100
	v_ashrrev_i32_e32 v5, 31, v4
	v_add_u32_e32 v89, s24, v6
	s_add_i32 s24, 0, 0x1e800
	v_add_u32_e32 v93, s8, v2
	v_add_u32_e32 v2, 0, v1
	s_mov_b32 s13, 0
	v_cmp_gt_i32_e64 s[6:7], s6, v54
	v_add_u32_e32 v90, s24, v6
	s_mov_b32 s47, -1
	v_lshlrev_b64 v[66:67], 2, v[4:5]
	v_lshlrev_b32_e32 v56, 2, v56
	s_mov_b64 s[14:15], 0x1000
	s_movk_i32 s27, 0x1000
	s_mov_b64 s[24:25], 0x1800
	v_add_u32_e32 v94, 0x16800, v2
	v_add_u32_e32 v95, 0x18800, v2
	v_add_u32_e32 v96, 0x1a800, v2
	s_mov_b32 s26, 0x3fb504f3
	v_mov_b32_e32 v97, 0x358637bd
	s_mov_b32 s34, 0xf800000
	v_mov_b32_e32 v98, 0x260
	s_mov_b64 s[36:37], 0x400
	s_mov_b32 s35, 0xbfb8aa3b
	s_mov_b32 s44, 0x42ce8ed0
	s_mov_b32 s45, 0xc2b17218
	v_add_u32_e32 v99, 0x1c800, v2
	v_add_u32_e32 v100, 0x1e800, v2
	v_mov_b32_e32 v101, 0x7f800000
	s_mov_b32 s46, s22
	s_load_dwordx2 s[84:85], s[10:11], 0x0
	s_load_dwordx2 s[86:87], s[10:11], 0x10
	s_waitcnt lgkmcnt(0)
	s_lshl_b32 s88, s22, 3
	s_add_i32 s88, s88, s3
	s_mov_b32 s89, 0
	s_lshl_b64 s[90:91], s[88:89], 12
	v_lshl_add_u64 v[240:241], v[58:59], 0, s[90:91]
	global_load_dwordx4 v[196:199], v[240:241], off
	global_load_dwordx4 v[200:203], v[240:241], off offset:1024
	global_load_dwordx4 v[220:223], v[240:241], off offset:2048
	global_load_dwordx4 v[232:235], v[240:241], off offset:3072
	s_add_i32 s94, s88, 0xffffc000
	s_cmpk_lt_i32 s88, 0x4000
	s_cselect_b32 s92, s84, s86
	s_cselect_b32 s93, s85, s87
	s_cselect_b32 s94, s88, s94
	s_mov_b32 s95, 0
	s_lshl_b64 s[94:95], s[94:95], 13
	s_add_u32 s92, s92, s94
	s_addc_u32 s93, s93, s95
	global_load_dwordx4 v[204:207], v56, s[92:93] offset:16
	global_load_dwordx4 v[208:211], v56, s[92:93]
	global_load_dwordx4 v[212:215], v56, s[92:93] offset:2064
	global_load_dwordx4 v[216:219], v56, s[92:93] offset:2048
	s_add_u32 s92, s92, 0x1000
	s_addc_u32 s93, s93, 0
	global_load_dwordx4 v[224:227], v56, s[92:93]
	global_load_dwordx4 v[228:231], v56, s[92:93] offset:16
	global_load_dwordx4 v[236:239], v56, s[92:93] offset:2048
	global_load_dwordx4 v[244:247], v56, s[92:93] offset:2064
	s_branch .LBB0_1215

; __device__ __forceinline__ void cvt8(const u32x4 r, float (&f)[8]) { f[0] = bflo(r.x); f[1] = bfhi(r.x); f[2] = bflo(r.y); f[3] = bfhi(r.y); f[4] = bflo(r.z); f[5] = bfhi(r.z); f[6] = bflo(r.w); f[7] = bfhi(r.w); }
; __device__ __forceinline__ void ph_post1(Ctx& C, int l, int nrows, bool dry = false) {
;     ...
;     for (int it = it0; it < it1; ++it, ++nit) {
;         const int row = it * 8 + C.wave;
;         const int mrow = row < NLAT ? row / SL : 4; const float* mod = WSP(float, WS_MOD) + (size_t)(l * 5 + mrow) * 12288;
;         __syncthreads();
;         if (mrow != cur_mrow) { stage2048(C, PAR, mod + 4096); stage2048(C, PAR + 2048, INP(I_LN1G) + l * DM); stage2048(C, PAR + 4096, INP(I_LN1B) + l * DM); stage2048(C, PAR + 6144, mod + 8192); stage2048(C, PAR + 8192, mod + 6144); cur_mrow = mrow; __syncthreads(); }
;         {
;             float v[32], y[32], g1[32];
;             if (l == 0) row_load(src_x0(C, row), C.lane, v); else row_load_bf16(WSP(bf16, WS_X) + (size_t)row * DM, C.lane, v);
;             row_load_lds(PAR, C.lane, g1);
;             { const bf16* yo = WSP(bf16, WS_YO) + (size_t)row * DM;
; #pragma unroll
;               for (int j = 0; j < 4; ++j) { float t8[8]; cvt8(*(const u32x4*)(yo + 512 * j + 8 * C.lane), t8);
; #pragma unroll
;                   for (int e = 0; e < 8; ++e) y[8 * j + e] = t8[e]; } }
.LBB0_1217:
	s_add_i32 s42, s8, 0xffffc000
	s_and_b64 s[38:39], s[38:39], exec
	s_cselect_b32 s38, s8, s42
	s_cselect_b32 s42, 0, 16
	s_cselect_b32 s39, s9, 0
	s_add_u32 s42, s10, s42
	s_addc_u32 s43, s11, 0
	s_lshl_b64 s[38:39], s[38:39], 13
	v_mov_b32_e32 v68, 0
	s_add_u32 s38, s42, s38
	s_addc_u32 s39, s43, s39
	s_lshl_b64 s[42:43], s[8:9], 12
	v_lshl_add_u64 v[170:171], v[58:59], 0, s[42:43]
	v_mov_b32_e32 v82, v196
	v_mov_b32_e32 v83, v197
	v_mov_b32_e32 v84, v198
	v_mov_b32_e32 v85, v199
	v_mov_b32_e32 v102, v200
	v_mov_b32_e32 v103, v201
	v_mov_b32_e32 v104, v202
	v_mov_b32_e32 v105, v203
	v_mov_b32_e32 v106, v204
	v_mov_b32_e32 v107, v205
	v_mov_b32_e32 v108, v206
	v_mov_b32_e32 v109, v207
	v_mov_b32_e32 v110, v208
	v_mov_b32_e32 v111, v209
	v_mov_b32_e32 v112, v210
	v_mov_b32_e32 v113, v211
	v_mov_b32_e32 v114, v212
	v_mov_b32_e32 v115, v213
	v_mov_b32_e32 v116, v214
	v_mov_b32_e32 v117, v215
	v_mov_b32_e32 v118, v216
	v_mov_b32_e32 v119, v217
	v_mov_b32_e32 v120, v218
	v_mov_b32_e32 v121, v219
	ds_read_b128 v[122:125], v94
	ds_read_b128 v[126:129], v94 offset:16
	ds_read_b128 v[130:133], v94 offset:2048
	ds_read_b128 v[134:137], v94 offset:2064
	ds_read_b128 v[138:141], v94 offset:4096
	ds_read_b128 v[142:145], v94 offset:4112
	ds_read_b128 v[50:53], v94 offset:6144
	ds_read_b128 v[146:149], v94 offset:6160
	ds_read_b128 v[74:77], v95
	ds_read_b128 v[78:81], v95 offset:16
	v_lshl_add_u64 v[172:173], s[38:39], 0, v[56:57]
	v_mov_b32_e32 v150, v220
	v_mov_b32_e32 v151, v221
	v_mov_b32_e32 v152, v222
	v_mov_b32_e32 v153, v223
	v_add_co_u32_e32 v174, vcc, s27, v172
	v_lshl_add_u64 v[2:3], v[172:173], 0, s[14:15]
	s_nop 0
	v_addc_co_u32_e32 v175, vcc, 0, v173, vcc
	v_mov_b32_e32 v154, v224
	v_mov_b32_e32 v155, v225
	v_mov_b32_e32 v156, v226
	v_mov_b32_e32 v157, v227
	v_mov_b32_e32 v158, v228
	v_mov_b32_e32 v159, v229
	v_mov_b32_e32 v160, v230
	v_mov_b32_e32 v161, v231
	ds_read_b128 v[162:165], v95 offset:2048
	ds_read_b128 v[166:169], v95 offset:2064
	ds_read_b128 v[42:45], v95 offset:4096
	ds_read_b128 v[46:49], v95 offset:4112
	ds_read_b128 v[38:41], v95 offset:6144
	ds_read_b128 v[2:5], v95 offset:6160
	ds_read_b128 v[34:37], v96
	ds_read_b128 v[30:33], v96 offset:16
	ds_read_b128 v[26:29], v96 offset:2048
	ds_read_b128 v[22:25], v96 offset:2064
	ds_read_b128 v[18:21], v96 offset:4096
	ds_read_b128 v[14:17], v96 offset:4112
	ds_read_b128 v[10:13], v96 offset:6144
	ds_read_b128 v[6:9], v96 offset:6160
	s_waitcnt lgkmcnt(14)
	v_pk_add_f32 v[70:71], v[78:79], 0 op_sel_hi:[1,0]
	v_pk_add_f32 v[72:73], v[76:77], 0 op_sel_hi:[1,0]
	v_pk_add_f32 v[76:77], v[80:81], 0 op_sel_hi:[1,0]
	s_waitcnt lgkmcnt(12)
	v_pk_add_f32 v[78:79], v[166:167], 0 op_sel_hi:[1,0]
	v_pk_add_f32 v[80:81], v[164:165], 0 op_sel_hi:[1,0]
	v_mov_b32_e32 v164, v232
	v_mov_b32_e32 v165, v233
	v_mov_b32_e32 v166, v234
	v_mov_b32_e32 v167, v235
	v_lshl_add_u64 v[176:177], v[172:173], 0, s[24:25]
	v_mov_b32_e32 v170, v236
	v_mov_b32_e32 v171, v237
	v_mov_b32_e32 v172, v238
	v_mov_b32_e32 v173, v239
	s_nop 0
	v_mov_b32_e32 v174, v244
	v_mov_b32_e32 v175, v245
	v_mov_b32_e32 v176, v246
	v_mov_b32_e32 v177, v247
	s_add_i32 s88, s46, 1
	s_cmp_ge_i32 s88, s12
	s_cbranch_scc1 .Lp1a_nopf
	s_add_i32 s88, s8, 8
	s_mov_b32 s89, 0
	s_lshl_b64 s[90:91], s[88:89], 12
	v_lshl_add_u64 v[240:241], v[58:59], 0, s[90:91]
	global_load_dwordx4 v[196:199], v[240:241], off
	global_load_dwordx4 v[200:203], v[240:241], off offset:1024
	global_load_dwordx4 v[220:223], v[240:241], off offset:2048
	global_load_dwordx4 v[232:235], v[240:241], off offset:3072
	s_add_i32 s94, s88, 0xffffc000
	s_cmpk_lt_i32 s88, 0x4000
	s_cselect_b32 s92, s84, s86
	s_cselect_b32 s93, s85, s87
	s_cselect_b32 s94, s88, s94
	s_mov_b32 s95, 0
	s_lshl_b64 s[94:95], s[94:95], 13
	s_add_u32 s92, s92, s94
	s_addc_u32 s93, s93, s95
	global_load_dwordx4 v[204:207], v56, s[92:93] offset:16
	global_load_dwordx4 v[208:211], v56, s[92:93]
	global_load_dwordx4 v[212:215], v56, s[92:93] offset:2064
	global_load_dwordx4 v[216:219], v56, s[92:93] offset:2048
	s_add_u32 s92, s92, 0x1000
	s_addc_u32 s93, s93, 0
	global_load_dwordx4 v[224:227], v56, s[92:93]
	global_load_dwordx4 v[228:231], v56, s[92:93] offset:16
	global_load_dwordx4 v[236:239], v56, s[92:93] offset:2048
	global_load_dwordx4 v[244:247], v56, s[92:93] offset:2064
; __device__ __forceinline__ float wave_sum(float v) { return xor32_sum(xor16_sum(row16_sum(v))); }
; __device__ __forceinline__ void row_ln(float (&v)[32]) {
;     float s = 0.f;
; #pragma unroll
;     for (int i = 0; i < 32; ++i) s += v[i];
;     const float mean = wave_sum(s) * (1.0f / DM); float q = 0.f;
; #pragma unroll
;     for (int i = 0; i < 32; ++i) { v[i] -= mean; q += v[i] * v[i]; }
;     const float rstd = 1.0f / sqrtf(wave_sum(q) * (1.0f / DM) + LN_EPS);
; __device__ __forceinline__ void ph_post1(Ctx& C, int l, int nrows, bool dry = false) {
;     ...
; #pragma unroll
;             for (int i = 0; i < 32; ++i) v[i] = ALPHA * v[i] + g1[i] * y[i];
;             row_ln(v); row_affine_lds(v, PAR + 2048, PAR + 4096, C.lane, 0.f);
.Lp1a_nopf:
	s_lshl_b64 s[38:39], s[8:9], 11
	v_pk_add_f32 v[74:75], v[74:75], 0 op_sel_hi:[1,0]
	s_waitcnt lgkmcnt(8)
	v_pk_add_f32 v[2:3], v[2:3], 0 op_sel_hi:[1,0]
	v_pk_add_f32 v[46:47], v[46:47], 0 op_sel_hi:[1,0]
	v_pk_add_f32 v[44:45], v[44:45], 0 op_sel_hi:[1,0]
	v_pk_add_f32 v[42:43], v[42:43], 0 op_sel_hi:[1,0]
	v_pk_add_f32 v[48:49], v[48:49], 0 op_sel_hi:[1,0]
	v_pk_add_f32 v[40:41], v[40:41], 0 op_sel_hi:[1,0]
	v_pk_add_f32 v[38:39], v[38:39], 0 op_sel_hi:[1,0]
	v_lshlrev_b32_e32 v178, 16, v85
	v_and_b32_e32 v179, 0xffff0000, v85
	v_lshlrev_b32_e32 v182, 16, v82
	v_and_b32_e32 v183, 0xffff0000, v82
	v_lshlrev_b32_e32 v180, 16, v84
	v_and_b32_e32 v181, 0xffff0000, v84
	v_lshlrev_b32_e32 v84, 16, v83
	v_and_b32_e32 v85, 0xffff0000, v83
	v_lshlrev_b32_e32 v82, 16, v105
	v_and_b32_e32 v83, 0xffff0000, v105
	v_lshlrev_b32_e32 v184, 16, v104
	v_and_b32_e32 v185, 0xffff0000, v104
	v_lshlrev_b32_e32 v104, 16, v103
	v_and_b32_e32 v105, 0xffff0000, v103
	v_lshlrev_b32_e32 v186, 16, v102
	v_and_b32_e32 v187, 0xffff0000, v102
	v_pk_mul_f32 v[102:103], v[128:129], v[178:179]
	v_pk_mul_f32 v[122:123], v[122:123], v[182:183]
	v_pk_fma_f32 v[102:103], v[108:109], s[26:27], v[102:103] op_sel_hi:[1,0,1]
	v_pk_fma_f32 v[108:109], v[110:111], s[26:27], v[122:123] op_sel_hi:[1,0,1]
	v_pk_mul_f32 v[84:85], v[124:125], v[84:85]
	v_add_f32_e32 v69, 0, v108
	v_pk_fma_f32 v[84:85], v[112:113], s[26:27], v[84:85] op_sel_hi:[1,0,1]
	v_add_f32_e32 v69, v109, v69
	v_pk_mul_f32 v[126:127], v[126:127], v[180:181]
	v_add_f32_e32 v69, v84, v69
	v_pk_fma_f32 v[106:107], v[106:107], s[26:27], v[126:127] op_sel_hi:[1,0,1]
	v_add_f32_e32 v69, v85, v69
	v_add_f32_e32 v69, v106, v69
	v_add_f32_e32 v69, v107, v69
	v_pk_mul_f32 v[124:125], v[134:135], v[184:185]
	v_pk_mul_f32 v[128:129], v[130:131], v[186:187]
	v_add_f32_e32 v69, v102, v69
	v_pk_fma_f32 v[112:113], v[114:115], s[26:27], v[124:125] op_sel_hi:[1,0,1]
	v_pk_fma_f32 v[114:115], v[118:119], s[26:27], v[128:129] op_sel_hi:[1,0,1]
	v_add_f32_e32 v69, v103, v69
	v_pk_mul_f32 v[104:105], v[132:133], v[104:105]
	v_add_f32_e32 v69, v114, v69
	v_pk_fma_f32 v[104:105], v[120:121], s[26:27], v[104:105] op_sel_hi:[1,0,1]
	v_add_f32_e32 v69, v115, v69
	v_add_f32_e32 v69, v104, v69
	v_add_f32_e32 v69, v105, v69
	v_pk_mul_f32 v[82:83], v[136:137], v[82:83]
	v_add_f32_e32 v69, v112, v69
	v_pk_fma_f32 v[110:111], v[116:117], s[26:27], v[82:83] op_sel_hi:[1,0,1]
	v_add_f32_e32 v69, v113, v69
	v_lshlrev_b32_e32 v124, 16, v150
	v_and_b32_e32 v125, 0xffff0000, v150
	v_add_f32_e32 v69, v110, v69
	v_pk_mul_f32 v[124:125], v[138:139], v[124:125]
	v_add_f32_e32 v69, v111, v69
	v_lshlrev_b32_e32 v122, 16, v151
	v_and_b32_e32 v123, 0xffff0000, v151
	v_pk_fma_f32 v[124:125], v[154:155], s[26:27], v[124:125] op_sel_hi:[1,0,1]
	v_pk_mul_f32 v[122:123], v[140:141], v[122:123]
	v_add_f32_e32 v69, v124, v69
	v_lshlrev_b32_e32 v120, 16, v152
	v_and_b32_e32 v121, 0xffff0000, v152
	v_pk_fma_f32 v[122:123], v[156:157], s[26:27], v[122:123] op_sel_hi:[1,0,1]
	v_add_f32_e32 v69, v125, v69
	v_pk_mul_f32 v[120:121], v[142:143], v[120:121]
	v_add_f32_e32 v69, v122, v69
	v_lshlrev_b32_e32 v118, 16, v153
	v_and_b32_e32 v119, 0xffff0000, v153
	v_pk_fma_f32 v[120:121], v[158:159], s[26:27], v[120:121] op_sel_hi:[1,0,1]
	v_add_f32_e32 v69, v123, v69
	v_pk_mul_f32 v[118:119], v[144:145], v[118:119]
	v_add_f32_e32 v69, v120, v69
	v_lshlrev_b32_e32 v130, 16, v165
	v_and_b32_e32 v131, 0xffff0000, v165
	v_pk_fma_f32 v[118:119], v[160:161], s[26:27], v[118:119] op_sel_hi:[1,0,1]
	v_add_f32_e32 v69, v121, v69
	v_pk_mul_f32 v[52:53], v[52:53], v[130:131]
	v_lshlrev_b32_e32 v130, 16, v164
	v_and_b32_e32 v131, 0xffff0000, v164
	v_add_f32_e32 v69, v118, v69
	v_pk_mul_f32 v[50:51], v[50:51], v[130:131]
	v_add_f32_e32 v69, v119, v69
	v_pk_fma_f32 v[50:51], v[170:171], s[26:27], v[50:51] op_sel_hi:[1,0,1]
	v_lshlrev_b32_e32 v128, 16, v166
	v_add_f32_e32 v69, v50, v69
	v_and_b32_e32 v129, 0xffff0000, v166
	v_pk_fma_f32 v[52:53], v[172:173], s[26:27], v[52:53] op_sel_hi:[1,0,1]
	v_add_f32_e32 v69, v51, v69
	v_pk_mul_f32 v[128:129], v[146:147], v[128:129]
	v_add_f32_e32 v69, v52, v69
	v_lshlrev_b32_e32 v126, 16, v167
	v_and_b32_e32 v127, 0xffff0000, v167
	v_pk_fma_f32 v[128:129], v[174:175], s[26:27], v[128:129] op_sel_hi:[1,0,1]
	v_add_f32_e32 v69, v53, v69
	v_pk_mul_f32 v[126:127], v[148:149], v[126:127]
	v_add_f32_e32 v69, v128, v69
	v_pk_fma_f32 v[126:127], v[176:177], s[26:27], v[126:127] op_sel_hi:[1,0,1]
	v_add_f32_e32 v69, v129, v69
	v_add_f32_e32 v69, v126, v69
	v_add_f32_e32 v69, v127, v69
	v_pk_add_f32 v[82:83], v[162:163], 0 op_sel_hi:[1,0]
	v_pk_add_f32 v[116:117], v[168:169], 0 op_sel_hi:[1,0]
	v_add_f32_dpp v69, v69, v69 quad_perm:[1,0,3,2] row_mask:0xf bank_mask:0xf bound_ctrl:1
	s_nop 1
	v_add_f32_dpp v69, v69, v69 quad_perm:[2,3,0,1] row_mask:0xf bank_mask:0xf bound_ctrl:1
	s_nop 1
	v_add_f32_dpp v69, v69, v69 row_half_mirror row_mask:0xf bank_mask:0xf bound_ctrl:1
	s_nop 1
	v_add_f32_dpp v69, v69, v69 row_mirror row_mask:0xf bank_mask:0xf bound_ctrl:1
	v_mov_b32_e32 v130, v69
	s_nop 1
	v_permlane16_swap_b32_e32 v69, v130
	v_add_f32_e32 v69, v69, v130
	v_mov_b32_e32 v130, v69
	s_nop 1
	v_permlane32_swap_b32_e32 v69, v130
	v_add_f32_e32 v69, v69, v130
	v_mul_f32_e32 v130, 0x3a000000, v69
	v_pk_add_f32 v[108:109], v[108:109], v[130:131] op_sel_hi:[1,0] neg_lo:[0,1] neg_hi:[0,1]
	v_pk_add_f32 v[84:85], v[84:85], v[130:131] op_sel_hi:[1,0] neg_lo:[0,1] neg_hi:[0,1]
	v_pk_mul_f32 v[132:133], v[108:109], v[108:109]
	v_pk_mul_f32 v[134:135], v[84:85], v[84:85]
	v_add_f32_e32 v69, v132, v133
	v_pk_add_f32 v[106:107], v[106:107], v[130:131] op_sel_hi:[1,0] neg_lo:[0,1] neg_hi:[0,1]
; #define LAS __attribute__((address_space(3)))
; __device__ __forceinline__ float wave_sum(float v) { return xor32_sum(xor16_sum(row16_sum(v))); }
; __device__ __forceinline__ void row_ln(float (&v)[32]) {
;     float s = 0.f;
; #pragma unroll
;     for (int i = 0; i < 32; ++i) s += v[i];
;     const float mean = wave_sum(s) * (1.0f / DM); float q = 0.f;
; #pragma unroll
;     for (int i = 0; i < 32; ++i) { v[i] -= mean; q += v[i] * v[i]; }
;     const float rstd = 1.0f / sqrtf(wave_sum(q) * (1.0f / DM) + LN_EPS);
; #pragma unroll
;     for (int i = 0; i < 32; ++i) v[i] *= rstd;
; }
; __device__ __forceinline__ void row_affine_lds(float (&v)[32], const LAS float* mul, const LAS float* add, int lane, float mul_off) {
;     float a[32], b[32]; row_load_lds(mul, lane, a); row_load_lds(add, lane, b);
; #pragma unroll
;     for (int i = 0; i < 32; ++i) v[i] = v[i] * (a[i] + mul_off) + b[i];
; }
	v_add_f32_e32 v69, v134, v69
	v_pk_mul_f32 v[136:137], v[106:107], v[106:107]
	v_add_f32_e32 v69, v135, v69
	v_pk_add_f32 v[102:103], v[102:103], v[130:131] op_sel_hi:[1,0] neg_lo:[0,1] neg_hi:[0,1]
	v_add_f32_e32 v69, v136, v69
	v_pk_mul_f32 v[138:139], v[102:103], v[102:103]
	v_add_f32_e32 v69, v137, v69
	v_pk_add_f32 v[114:115], v[114:115], v[130:131] op_sel_hi:[1,0] neg_lo:[0,1] neg_hi:[0,1]
	v_add_f32_e32 v69, v138, v69
	v_pk_mul_f32 v[140:141], v[114:115], v[114:115]
	v_add_f32_e32 v69, v139, v69
	v_pk_add_f32 v[104:105], v[104:105], v[130:131] op_sel_hi:[1,0] neg_lo:[0,1] neg_hi:[0,1]
	v_add_f32_e32 v69, v140, v69
	v_pk_mul_f32 v[142:143], v[104:105], v[104:105]
	v_add_f32_e32 v69, v141, v69
	v_pk_add_f32 v[112:113], v[112:113], v[130:131] op_sel_hi:[1,0] neg_lo:[0,1] neg_hi:[0,1]
	v_add_f32_e32 v69, v142, v69
	v_pk_mul_f32 v[144:145], v[112:113], v[112:113]
	v_add_f32_e32 v69, v143, v69
	v_pk_add_f32 v[110:111], v[110:111], v[130:131] op_sel_hi:[1,0] neg_lo:[0,1] neg_hi:[0,1]
	v_add_f32_e32 v69, v144, v69
	v_pk_mul_f32 v[146:147], v[110:111], v[110:111]
	v_add_f32_e32 v69, v145, v69
	v_pk_add_f32 v[124:125], v[124:125], v[130:131] op_sel_hi:[1,0] neg_lo:[0,1] neg_hi:[0,1]
	v_add_f32_e32 v69, v146, v69
	v_pk_mul_f32 v[148:149], v[124:125], v[124:125]
	v_add_f32_e32 v69, v147, v69
	v_pk_add_f32 v[122:123], v[122:123], v[130:131] op_sel_hi:[1,0] neg_lo:[0,1] neg_hi:[0,1]
	v_add_f32_e32 v69, v148, v69
	v_pk_mul_f32 v[150:151], v[122:123], v[122:123]
	v_add_f32_e32 v69, v149, v69
	v_pk_add_f32 v[120:121], v[120:121], v[130:131] op_sel_hi:[1,0] neg_lo:[0,1] neg_hi:[0,1]
	v_add_f32_e32 v69, v150, v69
	v_pk_mul_f32 v[152:153], v[120:121], v[120:121]
	v_add_f32_e32 v69, v151, v69
	v_pk_add_f32 v[118:119], v[118:119], v[130:131] op_sel_hi:[1,0] neg_lo:[0,1] neg_hi:[0,1]
	v_add_f32_e32 v69, v152, v69
	v_pk_mul_f32 v[154:155], v[118:119], v[118:119]
	v_add_f32_e32 v69, v153, v69
	v_pk_add_f32 v[50:51], v[50:51], v[130:131] op_sel_hi:[1,0] neg_lo:[0,1] neg_hi:[0,1]
	v_add_f32_e32 v69, v154, v69
	v_pk_mul_f32 v[156:157], v[50:51], v[50:51]
	v_add_f32_e32 v69, v155, v69
	v_pk_add_f32 v[52:53], v[52:53], v[130:131] op_sel_hi:[1,0] neg_lo:[0,1] neg_hi:[0,1]
	v_add_f32_e32 v69, v156, v69
	v_pk_mul_f32 v[158:159], v[52:53], v[52:53]
	v_add_f32_e32 v69, v157, v69
	v_pk_add_f32 v[128:129], v[128:129], v[130:131] op_sel_hi:[1,0] neg_lo:[0,1] neg_hi:[0,1]
	v_add_f32_e32 v69, v158, v69
	v_pk_mul_f32 v[160:161], v[128:129], v[128:129]
	v_add_f32_e32 v69, v159, v69
	v_pk_add_f32 v[126:127], v[126:127], v[130:131] op_sel_hi:[1,0] neg_lo:[0,1] neg_hi:[0,1]
	v_add_f32_e32 v69, v160, v69
	v_pk_mul_f32 v[130:131], v[126:127], v[126:127]
	v_add_f32_e32 v69, v161, v69
	v_add_f32_e32 v69, v130, v69
	v_add_f32_e32 v69, v131, v69
	s_nop 1
	v_add_f32_dpp v69, v69, v69 quad_perm:[1,0,3,2] row_mask:0xf bank_mask:0xf bound_ctrl:1
	s_nop 1
	v_add_f32_dpp v69, v69, v69 quad_perm:[2,3,0,1] row_mask:0xf bank_mask:0xf bound_ctrl:1
	s_nop 1
	v_add_f32_dpp v69, v69, v69 row_half_mirror row_mask:0xf bank_mask:0xf bound_ctrl:1
	s_nop 1
	v_add_f32_dpp v69, v69, v69 row_mirror row_mask:0xf bank_mask:0xf bound_ctrl:1
	v_mov_b32_e32 v130, v69
	s_nop 1
	v_permlane16_swap_b32_e32 v69, v130
	v_add_f32_e32 v69, v69, v130
	v_mov_b32_e32 v130, v69
	s_nop 1
	v_permlane32_swap_b32_e32 v69, v130
	v_add_f32_e32 v69, v69, v130
	v_fmamk_f32 v69, v69, 0x3a000000, v97
	v_mul_f32_e32 v130, 0x4f800000, v69
	v_cmp_gt_f32_e32 vcc, s34, v69
	s_nop 1
	v_cndmask_b32_e32 v69, v69, v130, vcc
	v_sqrt_f32_e32 v130, v69
	s_nop 0
	v_add_u32_e32 v131, -1, v130
	v_fma_f32 v132, -v131, v130, v69
	v_cmp_ge_f32_e64 s[8:9], 0, v132
	v_add_u32_e32 v132, 1, v130
	s_nop 0
	v_cndmask_b32_e64 v131, v130, v131, s[8:9]
	v_fma_f32 v130, -v132, v130, v69
	v_cmp_lt_f32_e64 s[8:9], 0, v130
	s_nop 1
	v_cndmask_b32_e64 v130, v131, v132, s[8:9]
	v_mul_f32_e32 v131, 0x37800000, v130
	v_cndmask_b32_e32 v130, v130, v131, vcc
	v_cmp_class_f32_e32 vcc, v69, v98
	s_nop 1
	v_cndmask_b32_e32 v69, v130, v69, vcc
	v_div_scale_f32 v130, s[8:9], v69, v69, 1.0
	v_rcp_f32_e32 v131, v130
	s_nop 0
	v_fma_f32 v132, -v130, v131, 1.0
	v_fmac_f32_e32 v131, v132, v131
	v_div_scale_f32 v132, vcc, 1.0, v69, 1.0
	v_mul_f32_e32 v133, v132, v131
	v_fma_f32 v134, -v130, v133, v132
	v_fmac_f32_e32 v133, v134, v131
	v_fma_f32 v130, -v130, v133, v132
	v_div_fmas_f32 v130, v130, v131, v133
	v_div_fixup_f32 v130, v130, v69, 1.0
	v_pk_mul_f32 v[108:109], v[108:109], v[130:131] op_sel_hi:[1,0]
	v_pk_mul_f32 v[84:85], v[84:85], v[130:131] op_sel_hi:[1,0]
	v_pk_mul_f32 v[106:107], v[106:107], v[130:131] op_sel_hi:[1,0]
	v_pk_mul_f32 v[102:103], v[102:103], v[130:131] op_sel_hi:[1,0]
	v_pk_mul_f32 v[128:129], v[128:129], v[130:131] op_sel_hi:[1,0]
	v_pk_mul_f32 v[114:115], v[114:115], v[130:131] op_sel_hi:[1,0]
	v_pk_mul_f32 v[104:105], v[104:105], v[130:131] op_sel_hi:[1,0]
	v_pk_mul_f32 v[112:113], v[112:113], v[130:131] op_sel_hi:[1,0]
	v_pk_mul_f32 v[110:111], v[110:111], v[130:131] op_sel_hi:[1,0]
	v_pk_mul_f32 v[126:127], v[126:127], v[130:131] op_sel_hi:[1,0]
	s_waitcnt lgkmcnt(7)
	v_pk_fma_f32 v[108:109], v[74:75], v[108:109], v[34:35]
	v_pk_fma_f32 v[84:85], v[72:73], v[84:85], v[36:37]
	s_waitcnt lgkmcnt(6)
	v_pk_fma_f32 v[106:107], v[70:71], v[106:107], v[30:31]
	v_pk_fma_f32 v[102:103], v[76:77], v[102:103], v[32:33]
	s_waitcnt lgkmcnt(0)
; __device__ __forceinline__ float wave_sum(float v) { return xor32_sum(xor16_sum(row16_sum(v))); }
; __device__ __forceinline__ void row_ln(float (&v)[32]) {
;     float s = 0.f;
; #pragma unroll
;     for (int i = 0; i < 32; ++i) s += v[i];
;     const float mean = wave_sum(s) * (1.0f / DM); float q = 0.f;
; #pragma unroll
;     for (int i = 0; i < 32; ++i) { v[i] -= mean; q += v[i] * v[i]; }
; __device__ __forceinline__ void ph_post1(Ctx& C, int l, int nrows, bool dry = false) {
;     ...
;             row_ln(v); row_affine_lds(v, PAR + 2048, PAR + 4096, C.lane, 0.f);
;             row_store_bf16(WSP(bf16, WS_X) + (size_t)row * DM, C.lane, v);
;             row_ln(v); row_affine_lds(v, PAR + 6144, PAR + 8192, C.lane, 1.0f);
	v_pk_fma_f32 v[128:129], v[128:129], v[2:3], v[6:7]
	v_pk_add_f32 v[2:3], v[4:5], 0 op_sel_hi:[1,0]
	v_pk_mul_f32 v[124:125], v[124:125], v[130:131] op_sel_hi:[1,0]
	v_pk_mul_f32 v[122:123], v[122:123], v[130:131] op_sel_hi:[1,0]
	v_pk_mul_f32 v[120:121], v[120:121], v[130:131] op_sel_hi:[1,0]
	v_pk_mul_f32 v[118:119], v[118:119], v[130:131] op_sel_hi:[1,0]
	v_pk_fma_f32 v[82:83], v[82:83], v[114:115], v[26:27]
	v_pk_fma_f32 v[104:105], v[80:81], v[104:105], v[28:29]
	v_pk_fma_f32 v[112:113], v[78:79], v[112:113], v[22:23]
	v_pk_fma_f32 v[110:111], v[116:117], v[110:111], v[24:25]
	v_pk_fma_f32 v[126:127], v[126:127], v[2:3], v[8:9]
	v_lshl_add_u64 v[6:7], v[60:61], 0, s[42:43]
	v_cvt_pk_bf16_f32 v2, v108, v109
	v_cvt_pk_bf16_f32 v3, v84, v85
	v_cvt_pk_bf16_f32 v4, v106, v107
	v_cvt_pk_bf16_f32 v5, v102, v103
	v_pk_mul_f32 v[50:51], v[50:51], v[130:131] op_sel_hi:[1,0]
	v_pk_mul_f32 v[52:53], v[52:53], v[130:131] op_sel_hi:[1,0]
	v_pk_fma_f32 v[114:115], v[42:43], v[124:125], v[18:19]
	v_pk_fma_f32 v[116:117], v[44:45], v[122:123], v[20:21]
	v_pk_fma_f32 v[120:121], v[46:47], v[120:121], v[14:15]
	v_pk_fma_f32 v[118:119], v[48:49], v[118:119], v[16:17]
	global_store_dwordx4 v[6:7], v[2:5], off
	v_pk_fma_f32 v[122:123], v[50:51], v[38:39], v[10:11]
	v_pk_fma_f32 v[124:125], v[52:53], v[40:41], v[12:13]
	v_cvt_pk_bf16_f32 v2, v82, v83
	v_cvt_pk_bf16_f32 v3, v104, v105
	v_cvt_pk_bf16_f32 v4, v112, v113
	v_cvt_pk_bf16_f32 v5, v110, v111
	global_store_dwordx4 v[6:7], v[2:5], off offset:1024
	s_nop 1
	v_cvt_pk_bf16_f32 v2, v114, v115
	v_cvt_pk_bf16_f32 v3, v116, v117
	v_cvt_pk_bf16_f32 v4, v120, v121
	v_cvt_pk_bf16_f32 v5, v118, v119
	global_store_dwordx4 v[6:7], v[2:5], off offset:2048
	s_nop 1
	v_cvt_pk_bf16_f32 v2, v122, v123
	v_cvt_pk_bf16_f32 v3, v124, v125
	v_cvt_pk_bf16_f32 v4, v128, v129
	v_cvt_pk_bf16_f32 v5, v126, v127
	global_store_dwordx4 v[6:7], v[2:5], off offset:3072
	s_nop 1
	v_add_f32_e32 v2, 0, v108
	v_add_f32_e32 v2, v109, v2
	v_add_f32_e32 v2, v84, v2
	v_add_f32_e32 v2, v85, v2
	v_add_f32_e32 v2, v106, v2
	v_add_f32_e32 v2, v107, v2
	v_add_f32_e32 v2, v102, v2
	v_add_f32_e32 v2, v103, v2
	v_add_f32_e32 v2, v82, v2
	v_add_f32_e32 v2, v83, v2
	v_add_f32_e32 v2, v104, v2
	v_add_f32_e32 v2, v105, v2
	v_add_f32_e32 v2, v112, v2
	v_add_f32_e32 v2, v113, v2
	v_add_f32_e32 v2, v110, v2
	v_add_f32_e32 v2, v111, v2
	v_add_f32_e32 v2, v114, v2
	v_add_f32_e32 v2, v115, v2
	v_add_f32_e32 v2, v116, v2
	v_add_f32_e32 v2, v117, v2
	v_add_f32_e32 v2, v120, v2
	v_add_f32_e32 v2, v121, v2
	v_add_f32_e32 v2, v118, v2
	v_add_f32_e32 v2, v119, v2
	v_add_f32_e32 v2, v122, v2
	v_add_f32_e32 v2, v123, v2
	v_add_f32_e32 v2, v124, v2
	v_add_f32_e32 v2, v125, v2
	v_add_f32_e32 v2, v128, v2
	v_add_f32_e32 v2, v129, v2
	v_add_f32_e32 v2, v126, v2
	v_add_f32_e32 v2, v127, v2
	s_nop 1
	v_add_f32_dpp v2, v2, v2 quad_perm:[1,0,3,2] row_mask:0xf bank_mask:0xf bound_ctrl:1
	s_nop 1
	v_add_f32_dpp v2, v2, v2 quad_perm:[2,3,0,1] row_mask:0xf bank_mask:0xf bound_ctrl:1
	s_nop 1
	v_add_f32_dpp v2, v2, v2 row_half_mirror row_mask:0xf bank_mask:0xf bound_ctrl:1
	s_nop 1
	v_add_f32_dpp v2, v2, v2 row_mirror row_mask:0xf bank_mask:0xf bound_ctrl:1
	v_mov_b32_e32 v3, v2
	s_nop 1
	v_permlane16_swap_b32_e32 v2, v3
	v_add_f32_e32 v2, v2, v3
	v_mov_b32_e32 v3, v2
	s_nop 1
	v_permlane32_swap_b32_e32 v2, v3
	v_add_f32_e32 v2, v2, v3
	v_mul_f32_e32 v130, 0x3a000000, v2
	v_pk_add_f32 v[108:109], v[108:109], v[130:131] op_sel_hi:[1,0] neg_lo:[0,1] neg_hi:[0,1]
	v_pk_add_f32 v[84:85], v[84:85], v[130:131] op_sel_hi:[1,0] neg_lo:[0,1] neg_hi:[0,1]
	v_pk_mul_f32 v[132:133], v[108:109], v[108:109]
	v_pk_mul_f32 v[134:135], v[84:85], v[84:85]
	v_add_f32_e32 v69, v132, v133
	v_pk_add_f32 v[106:107], v[106:107], v[130:131] op_sel_hi:[1,0] neg_lo:[0,1] neg_hi:[0,1]
	v_add_f32_e32 v69, v134, v69
	v_pk_mul_f32 v[136:137], v[106:107], v[106:107]
	v_add_f32_e32 v69, v135, v69
	v_pk_add_f32 v[102:103], v[102:103], v[130:131] op_sel_hi:[1,0] neg_lo:[0,1] neg_hi:[0,1]
	v_add_f32_e32 v69, v136, v69
	v_pk_mul_f32 v[138:139], v[102:103], v[102:103]
	v_add_f32_e32 v69, v137, v69
	v_pk_add_f32 v[82:83], v[82:83], v[130:131] op_sel_hi:[1,0] neg_lo:[0,1] neg_hi:[0,1]
	v_add_f32_e32 v69, v138, v69
	v_pk_mul_f32 v[140:141], v[82:83], v[82:83]
	v_add_f32_e32 v69, v139, v69
	v_pk_add_f32 v[104:105], v[104:105], v[130:131] op_sel_hi:[1,0] neg_lo:[0,1] neg_hi:[0,1]
	v_add_f32_e32 v69, v140, v69
	v_pk_mul_f32 v[142:143], v[104:105], v[104:105]
	v_add_f32_e32 v69, v141, v69
	v_pk_add_f32 v[112:113], v[112:113], v[130:131] op_sel_hi:[1,0] neg_lo:[0,1] neg_hi:[0,1]
	v_add_f32_e32 v69, v142, v69
	v_pk_mul_f32 v[144:145], v[112:113], v[112:113]
	v_add_f32_e32 v69, v143, v69
	v_pk_add_f32 v[110:111], v[110:111], v[130:131] op_sel_hi:[1,0] neg_lo:[0,1] neg_hi:[0,1]
	v_add_f32_e32 v69, v144, v69
	v_pk_mul_f32 v[146:147], v[110:111], v[110:111]
	v_add_f32_e32 v69, v145, v69
	v_pk_add_f32 v[114:115], v[114:115], v[130:131] op_sel_hi:[1,0] neg_lo:[0,1] neg_hi:[0,1]
	v_add_f32_e32 v69, v146, v69
	v_pk_mul_f32 v[148:149], v[114:115], v[114:115]
	v_add_f32_e32 v69, v147, v69
	v_pk_add_f32 v[116:117], v[116:117], v[130:131] op_sel_hi:[1,0] neg_lo:[0,1] neg_hi:[0,1]
	v_add_f32_e32 v69, v148, v69
	v_pk_mul_f32 v[150:151], v[116:117], v[116:117]
	v_add_f32_e32 v69, v149, v69
	v_pk_add_f32 v[120:121], v[120:121], v[130:131] op_sel_hi:[1,0] neg_lo:[0,1] neg_hi:[0,1]
	v_add_f32_e32 v69, v150, v69
	v_pk_mul_f32 v[152:153], v[120:121], v[120:121]
	v_add_f32_e32 v69, v151, v69
	v_pk_add_f32 v[118:119], v[118:119], v[130:131] op_sel_hi:[1,0] neg_lo:[0,1] neg_hi:[0,1]
	v_add_f32_e32 v69, v152, v69
	v_pk_mul_f32 v[154:155], v[118:119], v[118:119]
; #define LAS __attribute__((address_space(3)))
; __device__ __forceinline__ float wave_sum(float v) { return xor32_sum(xor16_sum(row16_sum(v))); }
; __device__ __forceinline__ void row_ln(float (&v)[32]) {
;     float s = 0.f;
; #pragma unroll
;     for (int i = 0; i < 32; ++i) s += v[i];
;     const float mean = wave_sum(s) * (1.0f / DM); float q = 0.f;
; #pragma unroll
;     for (int i = 0; i < 32; ++i) { v[i] -= mean; q += v[i] * v[i]; }
;     const float rstd = 1.0f / sqrtf(wave_sum(q) * (1.0f / DM) + LN_EPS);
; #pragma unroll
;     for (int i = 0; i < 32; ++i) v[i] *= rstd;
; }
; __device__ __forceinline__ void row_affine(float (&v)[32], const float* mul, const float* add, int lane, float mul_off) {
;     float a[32], b[32]; row_load(mul, lane, a); row_load(add, lane, b);
; #pragma unroll
;     for (int i = 0; i < 32; ++i) v[i] = v[i] * (a[i] + mul_off) + b[i];
; }
; __device__ __forceinline__ void row_load_lds(const LAS float* p, int lane, float (&v)[32]) {
; #pragma unroll
;     for (int j = 0; j < 4; ++j) { const f32x4 a = *(const LAS f32x4*)(p + 512 * j + 8 * lane), b = *(const LAS f32x4*)(p + 512 * j + 8 * lane + 4);
;         v[8 * j] = a[0]; v[8 * j + 1] = a[1]; v[8 * j + 2] = a[2]; v[8 * j + 3] = a[3]; v[8 * j + 4] = b[0]; v[8 * j + 5] = b[1]; v[8 * j + 6] = b[2]; v[8 * j + 7] = b[3]; }
; }
; __device__ __forceinline__ void row_affine_lds(float (&v)[32], const LAS float* mul, const LAS float* add, int lane, float mul_off) {
;     float a[32], b[32]; row_load_lds(mul, lane, a); row_load_lds(add, lane, b);
; #pragma unroll
;     for (int i = 0; i < 32; ++i) v[i] = v[i] * (a[i] + mul_off) + b[i];
; }
	v_add_f32_e32 v69, v153, v69
	v_pk_add_f32 v[122:123], v[122:123], v[130:131] op_sel_hi:[1,0] neg_lo:[0,1] neg_hi:[0,1]
	v_add_f32_e32 v69, v154, v69
	v_pk_mul_f32 v[156:157], v[122:123], v[122:123]
	v_add_f32_e32 v69, v155, v69
	v_pk_add_f32 v[124:125], v[124:125], v[130:131] op_sel_hi:[1,0] neg_lo:[0,1] neg_hi:[0,1]
	v_add_f32_e32 v69, v156, v69
	v_pk_mul_f32 v[158:159], v[124:125], v[124:125]
	v_add_f32_e32 v69, v157, v69
	v_pk_add_f32 v[128:129], v[128:129], v[130:131] op_sel_hi:[1,0] neg_lo:[0,1] neg_hi:[0,1]
	v_add_f32_e32 v69, v158, v69
	v_pk_mul_f32 v[160:161], v[128:129], v[128:129]
	v_add_f32_e32 v69, v159, v69
	v_pk_add_f32 v[126:127], v[126:127], v[130:131] op_sel_hi:[1,0] neg_lo:[0,1] neg_hi:[0,1]
	v_add_f32_e32 v69, v160, v69
	v_pk_mul_f32 v[130:131], v[126:127], v[126:127]
	v_add_f32_e32 v69, v161, v69
	v_add_f32_e32 v69, v130, v69
	v_add_f32_e32 v69, v131, v69
	ds_read_b128 v[2:5], v99
	ds_read_b128 v[6:9], v99 offset:16
	ds_read_b128 v[10:13], v99 offset:2048
	ds_read_b128 v[14:17], v99 offset:2064
	ds_read_b128 v[18:21], v99 offset:4096
	ds_read_b128 v[22:25], v99 offset:4112
	ds_read_b128 v[26:29], v99 offset:6144
	ds_read_b128 v[30:33], v99 offset:6160
	ds_read_b128 v[34:37], v100
	ds_read_b128 v[38:41], v100 offset:16
	ds_read_b128 v[42:45], v100 offset:2048
	ds_read_b128 v[46:49], v100 offset:2064
	ds_read_b128 v[50:53], v100 offset:4096
	ds_read_b128 v[70:73], v100 offset:4112
	ds_read_b128 v[74:77], v100 offset:6144
	ds_read_b128 v[78:81], v100 offset:6160
	v_add_f32_dpp v69, v69, v69 quad_perm:[1,0,3,2] row_mask:0xf bank_mask:0xf bound_ctrl:1
	s_waitcnt lgkmcnt(14)
	v_pk_add_f32 v[2:3], v[2:3], 1.0 op_sel_hi:[1,0]
	v_pk_add_f32 v[4:5], v[4:5], 1.0 op_sel_hi:[1,0]
	v_add_f32_dpp v69, v69, v69 quad_perm:[2,3,0,1] row_mask:0xf bank_mask:0xf bound_ctrl:1
	v_pk_add_f32 v[6:7], v[6:7], 1.0 op_sel_hi:[1,0]
	s_waitcnt lgkmcnt(13)
	v_pk_add_f32 v[10:11], v[10:11], 1.0 op_sel_hi:[1,0]
	v_add_f32_dpp v69, v69, v69 row_half_mirror row_mask:0xf bank_mask:0xf bound_ctrl:1
	s_waitcnt lgkmcnt(12)
	v_pk_add_f32 v[14:15], v[14:15], 1.0 op_sel_hi:[1,0]
	v_pk_add_f32 v[8:9], v[8:9], 1.0 op_sel_hi:[1,0]
	v_add_f32_dpp v69, v69, v69 row_mirror row_mask:0xf bank_mask:0xf bound_ctrl:1
	v_mov_b32_e32 v130, v69
	s_nop 1
	v_permlane16_swap_b32_e32 v69, v130
	v_add_f32_e32 v69, v69, v130
	v_mov_b32_e32 v130, v69
	s_nop 1
	v_permlane32_swap_b32_e32 v69, v130
	v_add_f32_e32 v69, v69, v130
	v_fmamk_f32 v69, v69, 0x3a000000, v97
	v_mul_f32_e32 v130, 0x4f800000, v69
	v_cmp_gt_f32_e32 vcc, s34, v69
	s_waitcnt lgkmcnt(11)
	v_pk_add_f32 v[18:19], v[18:19], 1.0 op_sel_hi:[1,0]
	s_waitcnt lgkmcnt(10)
	v_pk_add_f32 v[22:23], v[22:23], 1.0 op_sel_hi:[1,0]
	v_cndmask_b32_e32 v69, v69, v130, vcc
	v_sqrt_f32_e32 v130, v69
	s_waitcnt lgkmcnt(9)
	v_pk_add_f32 v[26:27], v[26:27], 1.0 op_sel_hi:[1,0]
	s_waitcnt lgkmcnt(8)
	v_pk_add_f32 v[30:31], v[30:31], 1.0 op_sel_hi:[1,0]
	v_pk_add_f32 v[12:13], v[12:13], 1.0 op_sel_hi:[1,0]
	v_add_u32_e32 v131, -1, v130
	v_fma_f32 v132, -v131, v130, v69
	v_cmp_ge_f32_e64 s[8:9], 0, v132
	v_add_u32_e32 v132, 1, v130
	v_pk_add_f32 v[16:17], v[16:17], 1.0 op_sel_hi:[1,0]
	v_cndmask_b32_e64 v131, v130, v131, s[8:9]
	v_fma_f32 v130, -v132, v130, v69
	v_cmp_lt_f32_e64 s[8:9], 0, v130
	v_pk_add_f32 v[20:21], v[20:21], 1.0 op_sel_hi:[1,0]
	v_pk_add_f32 v[24:25], v[24:25], 1.0 op_sel_hi:[1,0]
	v_cndmask_b32_e64 v130, v131, v132, s[8:9]
	v_mul_f32_e32 v131, 0x37800000, v130
	v_cndmask_b32_e32 v130, v130, v131, vcc
	v_cmp_class_f32_e32 vcc, v69, v98
	v_pk_add_f32 v[28:29], v[28:29], 1.0 op_sel_hi:[1,0]
	v_pk_add_f32 v[32:33], v[32:33], 1.0 op_sel_hi:[1,0]
	v_cndmask_b32_e32 v69, v130, v69, vcc
	v_div_scale_f32 v130, s[8:9], v69, v69, 1.0
	v_rcp_f32_e32 v131, v130
	s_mov_b32 s8, -4
	v_fma_f32 v132, -v130, v131, 1.0
	v_fmac_f32_e32 v131, v132, v131
	v_div_scale_f32 v132, vcc, 1.0, v69, 1.0
	v_mul_f32_e32 v133, v132, v131
	v_fma_f32 v134, -v130, v133, v132
	v_fmac_f32_e32 v133, v134, v131
	v_fma_f32 v130, -v130, v133, v132
	v_div_fmas_f32 v130, v130, v131, v133
	v_div_fixup_f32 v130, v130, v69, 1.0
	v_pk_mul_f32 v[108:109], v[108:109], v[130:131] op_sel_hi:[1,0]
	v_pk_mul_f32 v[84:85], v[84:85], v[130:131] op_sel_hi:[1,0]
	v_pk_mul_f32 v[106:107], v[106:107], v[130:131] op_sel_hi:[1,0]
	v_pk_mul_f32 v[82:83], v[82:83], v[130:131] op_sel_hi:[1,0]
	v_pk_mul_f32 v[112:113], v[112:113], v[130:131] op_sel_hi:[1,0]
	s_waitcnt lgkmcnt(7)
; #define LAS __attribute__((address_space(3)))
; __device__ __forceinline__ void ph_post1(Ctx& C, int l, int nrows, bool dry = false) {
;     ...
;             row_ln(v); row_affine_lds(v, PAR + 6144, PAR + 8192, C.lane, 1.0f);
;             row_store_fp8(WSP(unsigned char, WS_HB8) + (size_t)row * DM, C.lane, v);
; #pragma unroll
;             for (int j = 0; j < 4; ++j) { *(LAS f32x4*)(H2 + C.wave * DM + 512 * j + 8 * C.lane) = (f32x4){v[8 * j], v[8 * j + 1], v[8 * j + 2], v[8 * j + 3]};
;                 *(LAS f32x4*)(H2 + C.wave * DM + 512 * j + 8 * C.lane + 4) = (f32x4){v[8 * j + 4], v[8 * j + 5], v[8 * j + 6], v[8 * j + 7]}; }
;         }
;         __syncthreads();
;         {
;             const int e4 = C.lane & 7, cg = C.lane >> 3, cbase = 256 * C.wave + 32 * cg;
;             f32x2 acc[8][2];
; #pragma unroll
;             for (int r = 0; r < 8; ++r) { acc[r][0] = (f32x2){0.f, 0.f}; acc[r][1] = (f32x2){0.f, 0.f}; }
	v_pk_fma_f32 v[2:3], v[2:3], v[108:109], v[34:35]
	v_pk_fma_f32 v[4:5], v[4:5], v[84:85], v[36:37]
	s_waitcnt lgkmcnt(6)
	v_pk_fma_f32 v[6:7], v[6:7], v[106:107], v[38:39]
	v_mov_b32_e32 v36, 0
	v_mov_b32_e32 v37, 0
	v_pk_mul_f32 v[102:103], v[102:103], v[130:131] op_sel_hi:[1,0]
	v_pk_mul_f32 v[114:115], v[114:115], v[130:131] op_sel_hi:[1,0]
	v_pk_mul_f32 v[120:121], v[120:121], v[130:131] op_sel_hi:[1,0]
	s_waitcnt lgkmcnt(5)
	v_pk_fma_f32 v[10:11], v[10:11], v[82:83], v[42:43]
	s_waitcnt lgkmcnt(4)
	v_pk_fma_f32 v[14:15], v[14:15], v[112:113], v[46:47]
	v_cvt_pk_fp8_f32 v36, v2, v3
	v_cvt_pk_fp8_f32 v37, v6, v7
	v_mov_b32_e32 v38, 0
	v_mov_b32_e32 v39, 0
	v_pk_mul_f32 v[122:123], v[122:123], v[130:131] op_sel_hi:[1,0]
	v_pk_mul_f32 v[128:129], v[128:129], v[130:131] op_sel_hi:[1,0]
	v_pk_fma_f32 v[8:9], v[8:9], v[102:103], v[40:41]
	s_waitcnt lgkmcnt(3)
	v_pk_fma_f32 v[18:19], v[18:19], v[114:115], v[50:51]
	s_waitcnt lgkmcnt(2)
	v_pk_fma_f32 v[22:23], v[120:121], v[22:23], v[70:71]
	v_cvt_pk_fp8_f32 v38, v10, v11
	v_cvt_pk_fp8_f32 v39, v14, v15
	v_mov_b32_e32 v40, 0
	v_mov_b32_e32 v41, 0
	s_waitcnt lgkmcnt(1)
	v_pk_fma_f32 v[26:27], v[122:123], v[26:27], v[74:75]
	s_waitcnt lgkmcnt(0)
	v_pk_fma_f32 v[30:31], v[128:129], v[30:31], v[78:79]
	v_cvt_pk_fp8_f32 v40, v18, v19
	v_cvt_pk_fp8_f32 v41, v22, v23
	v_mov_b32_e32 v42, 0
	v_mov_b32_e32 v43, 0
	v_pk_mul_f32 v[104:105], v[104:105], v[130:131] op_sel_hi:[1,0]
	v_pk_mul_f32 v[110:111], v[110:111], v[130:131] op_sel_hi:[1,0]
	v_cvt_pk_fp8_f32 v42, v26, v27
	v_cvt_pk_fp8_f32 v43, v30, v31
	v_pk_mul_f32 v[116:117], v[116:117], v[130:131] op_sel_hi:[1,0]
	v_pk_mul_f32 v[118:119], v[118:119], v[130:131] op_sel_hi:[1,0]
	v_pk_fma_f32 v[12:13], v[12:13], v[104:105], v[44:45]
	v_pk_fma_f32 v[16:17], v[16:17], v[110:111], v[48:49]
	v_cvt_pk_fp8_f32 v36, v4, v5 op_sel:[0,0,1]
	v_cvt_pk_fp8_f32 v37, v8, v9 op_sel:[0,0,1]
	v_pk_mul_f32 v[124:125], v[124:125], v[130:131] op_sel_hi:[1,0]
	v_pk_mul_f32 v[126:127], v[126:127], v[130:131] op_sel_hi:[1,0]
	v_pk_fma_f32 v[20:21], v[20:21], v[116:117], v[52:53]
	v_pk_fma_f32 v[24:25], v[118:119], v[24:25], v[72:73]
	v_cvt_pk_fp8_f32 v38, v12, v13 op_sel:[0,0,1]
	v_cvt_pk_fp8_f32 v39, v16, v17 op_sel:[0,0,1]
	v_pk_fma_f32 v[28:29], v[124:125], v[28:29], v[76:77]
	v_pk_fma_f32 v[32:33], v[126:127], v[32:33], v[80:81]
	v_cvt_pk_fp8_f32 v40, v20, v21 op_sel:[0,0,1]
	v_cvt_pk_fp8_f32 v41, v24, v25 op_sel:[0,0,1]
	v_lshl_add_u64 v[34:35], v[62:63], 0, s[38:39]
	v_cvt_pk_fp8_f32 v42, v28, v29 op_sel:[0,0,1]
	v_cvt_pk_fp8_f32 v43, v32, v33 op_sel:[0,0,1]
	global_store_dwordx2 v[34:35], v[36:37], off
	global_store_dwordx2 v[34:35], v[38:39], off offset:512
	global_store_dwordx2 v[34:35], v[40:41], off offset:1024
	global_store_dwordx2 v[34:35], v[42:43], off offset:1536
	v_add_u32_e32 v34, s18, v1
	v_mov_b32_e32 v102, v93
	v_mov_b64_e32 v[74:75], v[64:65]
	v_mov_b32_e32 v69, v68
	v_mov_b32_e32 v38, v68
	v_mov_b32_e32 v39, v68
	v_mov_b32_e32 v40, v68
	v_mov_b32_e32 v41, v68
	v_mov_b32_e32 v42, v68
	v_mov_b32_e32 v43, v68
	v_mov_b32_e32 v44, v68
	v_mov_b32_e32 v45, v68
	v_mov_b32_e32 v46, v68
	v_mov_b32_e32 v47, v68
	v_mov_b32_e32 v48, v68
	v_mov_b32_e32 v49, v68
	v_mov_b32_e32 v50, v68
	v_mov_b32_e32 v51, v68
	v_mov_b32_e32 v52, v68
	v_mov_b32_e32 v53, v68
	v_mov_b32_e32 v70, v68
	v_mov_b32_e32 v71, v68
	v_mov_b32_e32 v72, v68
	v_mov_b32_e32 v73, v68
	v_mov_b32_e32 v76, v68
	v_mov_b32_e32 v77, v68
	v_mov_b32_e32 v78, v68
	v_mov_b32_e32 v79, v68
	v_mov_b32_e32 v80, v68
	v_mov_b32_e32 v81, v68
	v_mov_b32_e32 v82, v68
	v_mov_b32_e32 v83, v68
	v_mov_b32_e32 v84, v68
	v_mov_b32_e32 v85, v68
	ds_write_b128 v34, v[2:5]
	ds_write_b128 v34, v[6:9] offset:16
	ds_write_b128 v34, v[10:13] offset:2048
	ds_write_b128 v34, v[14:17] offset:2064
	ds_write_b128 v34, v[18:21] offset:4096
	ds_write_b128 v34, v[22:25] offset:4112
	ds_write_b128 v34, v[26:29] offset:6144
	ds_write_b128 v34, v[30:33] offset:6160
	s_waitcnt lgkmcnt(0)
	s_barrier

; __device__ __forceinline__ void cvt8(const u32x4 r, float (&f)[8]) { f[0] = bflo(r.x); f[1] = bfhi(r.x); f[2] = bflo(r.y); f[3] = bfhi(r.y); f[4] = bflo(r.z); f[5] = bfhi(r.z); f[6] = bflo(r.w); f[7] = bfhi(r.w); }
; __device__ __forceinline__ void ph_post1(Ctx& C, int l, int nrows, bool dry = false) {
;     ...
;     int nit = 0, cur_mrow = -1;
;     const int nit_all = nrows / 8, it0 = (int)(((long)C.bid * nit_all) / C.G), it1 = (int)(((long)(C.bid + 1) * nit_all) / C.G);
;     for (int it = it0; it < it1; ++it, ++nit) {
;         const int row = it * 8 + C.wave;
;         const int mrow = row < NLAT ? row / SL : 4; const float* mod = WSP(float, WS_MOD) + (size_t)(l * 5 + mrow) * 12288;
;         __syncthreads();
;         if (mrow != cur_mrow) { stage2048(C, PAR, mod + 4096); stage2048(C, PAR + 2048, INP(I_LN1G) + l * DM); stage2048(C, PAR + 4096, INP(I_LN1B) + l * DM); stage2048(C, PAR + 6144, mod + 8192); stage2048(C, PAR + 8192, mod + 6144); cur_mrow = mrow; __syncthreads(); }
;         {
;             float v[32], y[32], g1[32];
;             if (l == 0) row_load(src_x0(C, row), C.lane, v); else row_load_bf16(WSP(bf16, WS_X) + (size_t)row * DM, C.lane, v);
;             row_load_lds(PAR, C.lane, g1);
;             { const bf16* yo = WSP(bf16, WS_YO) + (size_t)row * DM;
; #pragma unroll
;               for (int j = 0; j < 4; ++j) { float t8[8]; cvt8(*(const u32x4*)(yo + 512 * j + 8 * C.lane), t8);
; #pragma unroll
;                   for (int e = 0; e < 8; ++e) y[8 * j + e] = t8[e]; } }
.LBB0_2347:
	s_cmp_ge_i32 s22, s12
	s_mov_b32 s4, 0
	s_cbranch_scc1 .LBB0_2389
	v_and_b32_e32 v8, 63, v62
	v_mov_b32_e32 v3, 0
	v_lshlrev_b32_e32 v4, 4, v8
	v_mov_b32_e32 v5, v3
	v_lshl_add_u64 v[6:7], s[20:21], 0, v[4:5]
	s_mov_b64 s[4:5], 0x29400000
	v_lshlrev_b32_e32 v2, 3, v8
	v_lshl_add_u64 v[64:65], v[6:7], 0, s[4:5]
	s_mov_b64 s[4:5], 0x46900000
	s_ashr_i32 s3, s3, 6
	v_lshl_add_u64 v[66:67], v[6:7], 0, s[4:5]
	v_lshl_add_u64 v[2:3], s[20:21], 0, v[2:3]
	s_mov_b64 s[4:5], 0x4f100000
	v_lshl_add_u64 v[68:69], v[2:3], 0, s[4:5]
	s_lshl_b32 s4, s3, 13
	s_lshl_b32 s14, s3, 10
	s_add_i32 s23, 0, 0x10000
	s_add_i32 s15, s4, 0
	v_lshlrev_b32_e32 v2, 2, v62
	s_add_i32 s6, s23, s14
	v_add_u32_e32 v63, s6, v4
	s_add_u32 s18, s20, 0x100000
	v_and_b32_e32 v4, 0xffffff80, v2
	v_and_b32_e32 v7, 0x7c, v2
	v_and_b32_e32 v5, 0xe0, v2
	s_load_dwordx2 s[8:9], s[10:11], 0xf0
	s_addc_u32 s19, s21, 0
	v_add3_u32 v99, s23, v4, v7
	s_add_i32 s23, 0, 0x14000
	v_add3_u32 v100, s23, v4, v7
	v_lshl_or_b32 v4, s3, 8, v5
	s_add_i32 s24, 0, 0x16800
	v_lshlrev_b32_e32 v6, 4, v62
	v_ashrrev_i32_e32 v5, 31, v4
	v_add_u32_e32 v94, s24, v6
	s_add_i32 s24, 0, 0x18800
	v_lshlrev_b64 v[4:5], 7, v[4:5]
	v_and_b32_e32 v7, 7, v62
	v_add_u32_e32 v95, s24, v6
	s_add_i32 s24, 0, 0x1a800
	v_lshl_or_b32 v4, v7, 4, v4
	v_lshlrev_b32_e32 v1, 5, v8
	v_ashrrev_i32_e32 v3, 31, v2
	v_add_u32_e32 v96, s24, v6
	s_add_i32 s24, 0, 0x1c800
	s_waitcnt lgkmcnt(0)
	v_lshl_add_u64 v[4:5], s[8:9], 0, v[4:5]
	s_mov_b64 s[8:9], 0x380
	s_movk_i32 s6, 0x100
	v_add_u32_e32 v97, s24, v6
	s_add_i32 s24, 0, 0x1e800
	v_lshl_add_u64 v[70:71], v[4:5], 0, s[8:9]
	v_and_b32_e32 v4, 0x380, v6
	s_add_i32 s8, s14, 0
	v_lshlrev_b64 v[72:73], 2, v[2:3]
	v_add_u32_e32 v2, 0, v1
	s_mov_b32 s13, 0
	v_cmp_gt_u32_e64 s[4:5], 8, v8
	v_cmp_gt_i32_e64 s[6:7], s6, v62
	v_add_u32_e32 v98, s24, v6
	v_add_u32_e32 v101, s8, v4
	s_mov_b32 s38, -1
	v_add_u32_e32 v102, 0x16800, v2
	v_add_u32_e32 v103, 0x18800, v2
	v_add_u32_e32 v104, 0x1a800, v2
	s_mov_b32 s14, 0x3fb504f3
	v_mov_b32_e32 v105, 0x358637bd
	s_mov_b32 s23, 0xf800000
	v_mov_b32_e32 v106, 0x260
	s_mov_b64 s[24:25], 0x400
	s_mov_b32 s34, 0xbfb8aa3b
	s_mov_b32 s35, 0x42ce8ed0
	s_mov_b32 s36, 0xc2b17218
	v_add_u32_e32 v107, 0x1c800, v2
	v_add_u32_e32 v108, 0x1e800, v2
	v_mov_b32_e32 v109, 0x7f800000
	s_mov_b32 s37, s22
	s_lshl_b32 s88, s22, 3
	s_add_i32 s88, s88, s3
	s_mov_b32 s89, 0
	s_lshl_b64 s[90:91], s[88:89], 12
	v_lshl_add_u64 v[228:229], v[64:65], 0, s[90:91]
	v_lshl_add_u64 v[230:231], v[66:67], 0, s[90:91]
	global_load_dwordx4 v[196:199], v[228:229], off
	global_load_dwordx4 v[200:203], v[230:231], off
	global_load_dwordx4 v[204:207], v[228:229], off offset:1024
	global_load_dwordx4 v[208:211], v[230:231], off offset:1024
	global_load_dwordx4 v[212:215], v[228:229], off offset:2048
	global_load_dwordx4 v[216:219], v[230:231], off offset:2048
	global_load_dwordx4 v[220:223], v[228:229], off offset:3072
	global_load_dwordx4 v[224:227], v[230:231], off offset:3072
	s_branch .LBB0_2350

; __device__ __forceinline__ void cvt8(const u32x4 r, float (&f)[8]) { f[0] = bflo(r.x); f[1] = bfhi(r.x); f[2] = bflo(r.y); f[3] = bfhi(r.y); f[4] = bflo(r.z); f[5] = bfhi(r.z); f[6] = bflo(r.w); f[7] = bfhi(r.w); }
; __device__ __forceinline__ void ph_post1(Ctx& C, int l, int nrows, bool dry = false) {
;     ...
;         {
;             float v[32], y[32], g1[32];
;             if (l == 0) row_load(src_x0(C, row), C.lane, v); else row_load_bf16(WSP(bf16, WS_X) + (size_t)row * DM, C.lane, v);
;             row_load_lds(PAR, C.lane, g1);
;             { const bf16* yo = WSP(bf16, WS_YO) + (size_t)row * DM;
; #pragma unroll
;               for (int j = 0; j < 4; ++j) { float t8[8]; cvt8(*(const u32x4*)(yo + 512 * j + 8 * C.lane), t8);
; #pragma unroll
;                   for (int e = 0; e < 8; ++e) y[8 * j + e] = t8[e]; } }
; #pragma unroll
;             for (int i = 0; i < 32; ++i) v[i] = ALPHA * v[i] + g1[i] * y[i];
;             row_ln(v); row_affine_lds(v, PAR + 2048, PAR + 4096, C.lane, 0.f);
.LBB0_2352:
	s_lshl_b64 s[26:27], s[8:9], 12
	v_lshl_add_u64 v[76:77], v[64:65], 0, s[26:27]
	v_mov_b32_e32 v90, v196
	v_mov_b32_e32 v91, v197
	v_mov_b32_e32 v92, v198
	v_mov_b32_e32 v93, v199
	v_lshl_add_u64 v[78:79], v[66:67], 0, s[26:27]
	v_mov_b32_e32 v110, v200
	v_mov_b32_e32 v111, v201
	v_mov_b32_e32 v112, v202
	v_mov_b32_e32 v113, v203
	v_mov_b32_e32 v114, v204
	v_mov_b32_e32 v115, v205
	v_mov_b32_e32 v116, v206
	v_mov_b32_e32 v117, v207
	v_mov_b32_e32 v118, v208
	v_mov_b32_e32 v119, v209
	v_mov_b32_e32 v120, v210
	v_mov_b32_e32 v121, v211
	ds_read_b128 v[122:125], v102
	ds_read_b128 v[126:129], v102 offset:16
	ds_read_b128 v[130:133], v102 offset:2048
	ds_read_b128 v[134:137], v102 offset:2064
	ds_read_b128 v[58:61], v102 offset:4096
	ds_read_b128 v[138:141], v102 offset:4112
	ds_read_b128 v[50:53], v102 offset:6144
	ds_read_b128 v[54:57], v102 offset:6160
	ds_read_b128 v[82:85], v103
	ds_read_b128 v[86:89], v103 offset:16
	ds_read_b128 v[142:145], v103 offset:2048
	ds_read_b128 v[146:149], v103 offset:2064
	ds_read_b128 v[42:45], v103 offset:4096
	ds_read_b128 v[46:49], v103 offset:4112
	ds_read_b128 v[38:41], v103 offset:6144
	ds_read_b128 v[2:5], v103 offset:6160
	ds_read_b128 v[34:37], v104
	ds_read_b128 v[30:33], v104 offset:16
	ds_read_b128 v[26:29], v104 offset:2048
	ds_read_b128 v[18:21], v104 offset:2064
	v_mov_b32_e32 v150, v212
	v_mov_b32_e32 v151, v213
	v_mov_b32_e32 v152, v214
	v_mov_b32_e32 v153, v215
	ds_read_b128 v[22:25], v104 offset:4096
	ds_read_b128 v[14:17], v104 offset:4112
	v_mov_b32_e32 v154, v216
	v_mov_b32_e32 v155, v217
	v_mov_b32_e32 v156, v218
	v_mov_b32_e32 v157, v219
	ds_read_b128 v[10:13], v104 offset:6144
	ds_read_b128 v[6:9], v104 offset:6160
	v_mov_b32_e32 v158, v220
	v_mov_b32_e32 v159, v221
	v_mov_b32_e32 v160, v222
	v_mov_b32_e32 v161, v223
	v_mov_b32_e32 v162, v224
	v_mov_b32_e32 v163, v225
	v_mov_b32_e32 v164, v226
	v_mov_b32_e32 v165, v227
	s_add_i32 s88, s37, 1
	s_cmp_ge_i32 s88, s12
	s_cbranch_scc1 .Lp1b_nopf
	s_add_i32 s88, s8, 8
	s_mov_b32 s89, 0
	s_lshl_b64 s[90:91], s[88:89], 12
	v_lshl_add_u64 v[228:229], v[64:65], 0, s[90:91]
	v_lshl_add_u64 v[230:231], v[66:67], 0, s[90:91]
	global_load_dwordx4 v[196:199], v[228:229], off
	global_load_dwordx4 v[200:203], v[230:231], off
	global_load_dwordx4 v[204:207], v[228:229], off offset:1024
	global_load_dwordx4 v[208:211], v[230:231], off offset:1024
	global_load_dwordx4 v[212:215], v[228:229], off offset:2048
	global_load_dwordx4 v[216:219], v[230:231], off offset:2048
	global_load_dwordx4 v[220:223], v[228:229], off offset:3072
	global_load_dwordx4 v[224:227], v[230:231], off offset:3072
.Lp1b_nopf:
	s_waitcnt lgkmcnt(14)
	v_pk_add_f32 v[78:79], v[86:87], 0 op_sel_hi:[1,0]
	v_pk_add_f32 v[80:81], v[84:85], 0 op_sel_hi:[1,0]
	v_pk_add_f32 v[84:85], v[88:89], 0 op_sel_hi:[1,0]
	s_waitcnt lgkmcnt(12)
	v_pk_add_f32 v[86:87], v[146:147], 0 op_sel_hi:[1,0]
	v_pk_add_f32 v[88:89], v[144:145], 0 op_sel_hi:[1,0]
	s_lshl_b64 s[26:27], s[8:9], 11
	v_pk_add_f32 v[82:83], v[82:83], 0 op_sel_hi:[1,0]
	s_waitcnt lgkmcnt(8)
	v_pk_add_f32 v[2:3], v[2:3], 0 op_sel_hi:[1,0]
	v_pk_add_f32 v[46:47], v[46:47], 0 op_sel_hi:[1,0]
	v_pk_add_f32 v[44:45], v[44:45], 0 op_sel_hi:[1,0]
	v_pk_add_f32 v[42:43], v[42:43], 0 op_sel_hi:[1,0]
	v_pk_add_f32 v[48:49], v[48:49], 0 op_sel_hi:[1,0]
	v_pk_add_f32 v[40:41], v[40:41], 0 op_sel_hi:[1,0]
	v_pk_add_f32 v[38:39], v[38:39], 0 op_sel_hi:[1,0]
	v_mov_b32_e32 v74, 0
	v_lshlrev_b32_e32 v146, 16, v113
	v_lshlrev_b32_e32 v144, 16, v93
	v_and_b32_e32 v145, 0xffff0000, v93
	v_and_b32_e32 v147, 0xffff0000, v113
	v_lshlrev_b32_e32 v166, 16, v92
	v_and_b32_e32 v167, 0xffff0000, v92
	v_lshlrev_b32_e32 v92, 16, v112
	v_and_b32_e32 v93, 0xffff0000, v112
	v_lshlrev_b32_e32 v112, 16, v91
	v_and_b32_e32 v113, 0xffff0000, v91
	v_lshlrev_b32_e32 v168, 16, v111
	v_and_b32_e32 v169, 0xffff0000, v111
	v_lshlrev_b32_e32 v170, 16, v90
	v_and_b32_e32 v171, 0xffff0000, v90
	v_lshlrev_b32_e32 v90, 16, v110
	v_and_b32_e32 v91, 0xffff0000, v110
	v_pk_mul_f32 v[124:125], v[124:125], v[168:169]
	v_pk_mul_f32 v[90:91], v[122:123], v[90:91]
	v_pk_fma_f32 v[112:113], v[112:113], s[14:15], v[124:125] op_sel_hi:[1,0,1]
	v_pk_fma_f32 v[124:125], v[170:171], s[14:15], v[90:91] op_sel_hi:[1,0,1]
	v_lshlrev_b32_e32 v176, 16, v119
	v_add_f32_e32 v75, 0, v124
	v_add_f32_e32 v75, v125, v75
	v_and_b32_e32 v177, 0xffff0000, v119
	v_pk_mul_f32 v[92:93], v[126:127], v[92:93]
	v_add_f32_e32 v75, v112, v75
	v_pk_mul_f32 v[126:127], v[132:133], v[176:177]
	v_pk_fma_f32 v[132:133], v[166:167], s[14:15], v[92:93] op_sel_hi:[1,0,1]
	v_add_f32_e32 v75, v113, v75
	v_pk_mul_f32 v[128:129], v[128:129], v[146:147]
	v_add_f32_e32 v75, v132, v75
	v_pk_fma_f32 v[128:129], v[144:145], s[14:15], v[128:129] op_sel_hi:[1,0,1]
	v_add_f32_e32 v75, v133, v75
	v_lshlrev_b32_e32 v92, 16, v118
	v_and_b32_e32 v93, 0xffff0000, v118
	v_add_f32_e32 v75, v128, v75
	v_lshlrev_b32_e32 v90, 16, v114
	v_and_b32_e32 v91, 0xffff0000, v114
	v_pk_mul_f32 v[92:93], v[130:131], v[92:93]
	v_lshlrev_b32_e32 v110, 16, v117
	v_and_b32_e32 v111, 0xffff0000, v117
	v_lshlrev_b32_e32 v172, 16, v121
	v_and_b32_e32 v173, 0xffff0000, v121
	v_lshlrev_b32_e32 v174, 16, v116
	v_and_b32_e32 v175, 0xffff0000, v116
	v_lshlrev_b32_e32 v116, 16, v120
	v_and_b32_e32 v117, 0xffff0000, v120
	v_lshlrev_b32_e32 v120, 16, v115
	v_and_b32_e32 v121, 0xffff0000, v115
	v_add_f32_e32 v75, v129, v75
	v_pk_fma_f32 v[114:115], v[90:91], s[14:15], v[92:93] op_sel_hi:[1,0,1]
	v_pk_mul_f32 v[122:123], v[136:137], v[172:173]
	v_add_f32_e32 v75, v114, v75
	v_pk_fma_f32 v[120:121], v[120:121], s[14:15], v[126:127] op_sel_hi:[1,0,1]
; __device__ __forceinline__ float wave_sum(float v) { return xor32_sum(xor16_sum(row16_sum(v))); }
; __device__ __forceinline__ void row_ln(float (&v)[32]) {
;     float s = 0.f;
; #pragma unroll
;     for (int i = 0; i < 32; ++i) s += v[i];
;     const float mean = wave_sum(s) * (1.0f / DM); float q = 0.f;
; #pragma unroll
;     for (int i = 0; i < 32; ++i) { v[i] -= mean; q += v[i] * v[i]; }
;     const float rstd = 1.0f / sqrtf(wave_sum(q) * (1.0f / DM) + LN_EPS);
; __device__ __forceinline__ void ph_post1(Ctx& C, int l, int nrows, bool dry = false) {
;     ...
; #pragma unroll
;             for (int i = 0; i < 32; ++i) v[i] = ALPHA * v[i] + g1[i] * y[i];
;             row_ln(v); row_affine_lds(v, PAR + 2048, PAR + 4096, C.lane, 0.f);
	v_add_f32_e32 v75, v115, v75
	v_pk_mul_f32 v[116:117], v[134:135], v[116:117]
	v_pk_fma_f32 v[110:111], v[110:111], s[14:15], v[122:123] op_sel_hi:[1,0,1]
	v_add_f32_e32 v75, v120, v75
	v_lshlrev_b32_e32 v122, 16, v157
	v_and_b32_e32 v123, 0xffff0000, v157
	v_pk_fma_f32 v[116:117], v[174:175], s[14:15], v[116:117] op_sel_hi:[1,0,1]
	v_add_f32_e32 v75, v121, v75
	v_lshlrev_b32_e32 v118, 16, v153
	v_and_b32_e32 v119, 0xffff0000, v153
	v_pk_mul_f32 v[122:123], v[140:141], v[122:123]
	v_lshlrev_b32_e32 v126, 16, v156
	v_and_b32_e32 v127, 0xffff0000, v156
	v_add_f32_e32 v75, v116, v75
	v_pk_fma_f32 v[118:119], v[118:119], s[14:15], v[122:123] op_sel_hi:[1,0,1]
	v_lshlrev_b32_e32 v122, 16, v152
	v_and_b32_e32 v123, 0xffff0000, v152
	v_pk_mul_f32 v[126:127], v[138:139], v[126:127]
	v_lshlrev_b32_e32 v130, 16, v155
	v_and_b32_e32 v131, 0xffff0000, v155
	v_add_f32_e32 v75, v117, v75
	v_pk_fma_f32 v[122:123], v[122:123], s[14:15], v[126:127] op_sel_hi:[1,0,1]
	v_lshlrev_b32_e32 v126, 16, v151
	v_and_b32_e32 v127, 0xffff0000, v151
	v_pk_mul_f32 v[60:61], v[60:61], v[130:131]
	v_lshlrev_b32_e32 v130, 16, v154
	v_and_b32_e32 v131, 0xffff0000, v154
	v_add_f32_e32 v75, v110, v75
	v_pk_fma_f32 v[60:61], v[126:127], s[14:15], v[60:61] op_sel_hi:[1,0,1]
	v_lshlrev_b32_e32 v126, 16, v150
	v_and_b32_e32 v127, 0xffff0000, v150
	v_pk_mul_f32 v[58:59], v[58:59], v[130:131]
	v_add_f32_e32 v75, v111, v75
	v_pk_fma_f32 v[58:59], v[126:127], s[14:15], v[58:59] op_sel_hi:[1,0,1]
	v_lshlrev_b32_e32 v130, 16, v165
	v_add_f32_e32 v75, v58, v75
	v_add_f32_e32 v75, v59, v75
	v_add_f32_e32 v75, v60, v75
	v_and_b32_e32 v131, 0xffff0000, v165
	v_add_f32_e32 v75, v61, v75
	v_lshlrev_b32_e32 v126, 16, v161
	v_and_b32_e32 v127, 0xffff0000, v161
	v_pk_mul_f32 v[56:57], v[56:57], v[130:131]
	v_lshlrev_b32_e32 v130, 16, v164
	v_and_b32_e32 v131, 0xffff0000, v164
	v_add_f32_e32 v75, v122, v75
	v_pk_fma_f32 v[56:57], v[126:127], s[14:15], v[56:57] op_sel_hi:[1,0,1]
	v_lshlrev_b32_e32 v126, 16, v160
	v_and_b32_e32 v127, 0xffff0000, v160
	v_pk_mul_f32 v[54:55], v[54:55], v[130:131]
	v_lshlrev_b32_e32 v130, 16, v163
	v_and_b32_e32 v131, 0xffff0000, v163
	v_add_f32_e32 v75, v123, v75
	v_pk_fma_f32 v[54:55], v[126:127], s[14:15], v[54:55] op_sel_hi:[1,0,1]
	v_lshlrev_b32_e32 v126, 16, v159
	v_and_b32_e32 v127, 0xffff0000, v159
	v_pk_mul_f32 v[52:53], v[52:53], v[130:131]
	v_lshlrev_b32_e32 v130, 16, v162
	v_and_b32_e32 v131, 0xffff0000, v162
	v_add_f32_e32 v75, v118, v75
	v_pk_fma_f32 v[52:53], v[126:127], s[14:15], v[52:53] op_sel_hi:[1,0,1]
	v_lshlrev_b32_e32 v126, 16, v158
	v_and_b32_e32 v127, 0xffff0000, v158
	v_pk_mul_f32 v[50:51], v[50:51], v[130:131]
	v_add_f32_e32 v75, v119, v75
	v_pk_fma_f32 v[50:51], v[126:127], s[14:15], v[50:51] op_sel_hi:[1,0,1]
	v_pk_add_f32 v[90:91], v[142:143], 0 op_sel_hi:[1,0]
	v_add_f32_e32 v75, v50, v75
	v_add_f32_e32 v75, v51, v75
	v_add_f32_e32 v75, v52, v75
	v_add_f32_e32 v75, v53, v75
	v_add_f32_e32 v75, v54, v75
	v_add_f32_e32 v75, v55, v75
	v_add_f32_e32 v75, v56, v75
	v_add_f32_e32 v75, v57, v75
	v_pk_add_f32 v[92:93], v[148:149], 0 op_sel_hi:[1,0]
	s_nop 0
	v_add_f32_dpp v75, v75, v75 quad_perm:[1,0,3,2] row_mask:0xf bank_mask:0xf bound_ctrl:1
	s_nop 1
	v_add_f32_dpp v75, v75, v75 quad_perm:[2,3,0,1] row_mask:0xf bank_mask:0xf bound_ctrl:1
	s_nop 1
	v_add_f32_dpp v75, v75, v75 row_half_mirror row_mask:0xf bank_mask:0xf bound_ctrl:1
	s_nop 1
	v_add_f32_dpp v75, v75, v75 row_mirror row_mask:0xf bank_mask:0xf bound_ctrl:1
	v_mov_b32_e32 v126, v75
	s_nop 1
	v_permlane16_swap_b32_e32 v75, v126
	v_add_f32_e32 v75, v75, v126
	v_mov_b32_e32 v126, v75
	s_nop 1
	v_permlane32_swap_b32_e32 v75, v126
	v_add_f32_e32 v75, v75, v126
	v_mul_f32_e32 v126, 0x3a000000, v75
	v_pk_add_f32 v[124:125], v[124:125], v[126:127] op_sel_hi:[1,0] neg_lo:[0,1] neg_hi:[0,1]
	v_pk_add_f32 v[112:113], v[112:113], v[126:127] op_sel_hi:[1,0] neg_lo:[0,1] neg_hi:[0,1]
	v_pk_mul_f32 v[130:131], v[124:125], v[124:125]
	v_pk_mul_f32 v[134:135], v[112:113], v[112:113]
	v_add_f32_e32 v75, v130, v131
	v_pk_add_f32 v[132:133], v[132:133], v[126:127] op_sel_hi:[1,0] neg_lo:[0,1] neg_hi:[0,1]
	v_add_f32_e32 v75, v134, v75
	v_pk_mul_f32 v[136:137], v[132:133], v[132:133]
	v_add_f32_e32 v75, v135, v75
	v_pk_add_f32 v[128:129], v[128:129], v[126:127] op_sel_hi:[1,0] neg_lo:[0,1] neg_hi:[0,1]
	v_add_f32_e32 v75, v136, v75
	v_pk_mul_f32 v[138:139], v[128:129], v[128:129]
	v_add_f32_e32 v75, v137, v75
	v_pk_add_f32 v[114:115], v[114:115], v[126:127] op_sel_hi:[1,0] neg_lo:[0,1] neg_hi:[0,1]
	v_add_f32_e32 v75, v138, v75
	v_pk_mul_f32 v[140:141], v[114:115], v[114:115]
	v_add_f32_e32 v75, v139, v75
	v_pk_add_f32 v[120:121], v[120:121], v[126:127] op_sel_hi:[1,0] neg_lo:[0,1] neg_hi:[0,1]
	v_add_f32_e32 v75, v140, v75
	v_pk_mul_f32 v[142:143], v[120:121], v[120:121]
	v_add_f32_e32 v75, v141, v75
	v_pk_add_f32 v[116:117], v[116:117], v[126:127] op_sel_hi:[1,0] neg_lo:[0,1] neg_hi:[0,1]
	v_add_f32_e32 v75, v142, v75
	v_pk_mul_f32 v[144:145], v[116:117], v[116:117]
	v_add_f32_e32 v75, v143, v75
	v_pk_add_f32 v[110:111], v[110:111], v[126:127] op_sel_hi:[1,0] neg_lo:[0,1] neg_hi:[0,1]
	v_add_f32_e32 v75, v144, v75
	v_pk_mul_f32 v[146:147], v[110:111], v[110:111]
	v_add_f32_e32 v75, v145, v75
	v_pk_add_f32 v[58:59], v[58:59], v[126:127] op_sel_hi:[1,0] neg_lo:[0,1] neg_hi:[0,1]
	v_add_f32_e32 v75, v146, v75
	v_pk_mul_f32 v[148:149], v[58:59], v[58:59]
	v_add_f32_e32 v75, v147, v75
	v_pk_add_f32 v[60:61], v[60:61], v[126:127] op_sel_hi:[1,0] neg_lo:[0,1] neg_hi:[0,1]
	v_add_f32_e32 v75, v148, v75
	v_pk_mul_f32 v[150:151], v[60:61], v[60:61]
	v_add_f32_e32 v75, v149, v75
; #define LAS __attribute__((address_space(3)))
; __device__ __forceinline__ float wave_sum(float v) { return xor32_sum(xor16_sum(row16_sum(v))); }
; __device__ __forceinline__ void row_ln(float (&v)[32]) {
;     ...
;     for (int i = 0; i < 32; ++i) { v[i] -= mean; q += v[i] * v[i]; }
;     const float rstd = 1.0f / sqrtf(wave_sum(q) * (1.0f / DM) + LN_EPS);
; #pragma unroll
;     for (int i = 0; i < 32; ++i) v[i] *= rstd;
; }
; __device__ __forceinline__ void row_affine(float (&v)[32], const float* mul, const float* add, int lane, float mul_off) {
;     float a[32], b[32]; row_load(mul, lane, a); row_load(add, lane, b);
; #pragma unroll
;     for (int i = 0; i < 32; ++i) v[i] = v[i] * (a[i] + mul_off) + b[i];
; }
; __device__ __forceinline__ void row_load_lds(const LAS float* p, int lane, float (&v)[32]) {
; #pragma unroll
;     for (int j = 0; j < 4; ++j) { const f32x4 a = *(const LAS f32x4*)(p + 512 * j + 8 * lane), b = *(const LAS f32x4*)(p + 512 * j + 8 * lane + 4);
;         v[8 * j] = a[0]; v[8 * j + 1] = a[1]; v[8 * j + 2] = a[2]; v[8 * j + 3] = a[3]; v[8 * j + 4] = b[0]; v[8 * j + 5] = b[1]; v[8 * j + 6] = b[2]; v[8 * j + 7] = b[3]; }
; }
; __device__ __forceinline__ void row_affine_lds(float (&v)[32], const LAS float* mul, const LAS float* add, int lane, float mul_off) {
;     float a[32], b[32]; row_load_lds(mul, lane, a); row_load_lds(add, lane, b);
; #pragma unroll
;     for (int i = 0; i < 32; ++i) v[i] = v[i] * (a[i] + mul_off) + b[i];
; }
; __device__ __forceinline__ void ph_post1(Ctx& C, int l, int nrows, bool dry = false) {
;     ...
;             row_ln(v); row_affine_lds(v, PAR + 2048, PAR + 4096, C.lane, 0.f);
;             row_store_bf16(WSP(bf16, WS_X) + (size_t)row * DM, C.lane, v);
	v_pk_add_f32 v[122:123], v[122:123], v[126:127] op_sel_hi:[1,0] neg_lo:[0,1] neg_hi:[0,1]
	v_add_f32_e32 v75, v150, v75
	v_pk_mul_f32 v[152:153], v[122:123], v[122:123]
	v_add_f32_e32 v75, v151, v75
	v_pk_add_f32 v[118:119], v[118:119], v[126:127] op_sel_hi:[1,0] neg_lo:[0,1] neg_hi:[0,1]
	v_add_f32_e32 v75, v152, v75
	v_pk_mul_f32 v[154:155], v[118:119], v[118:119]
	v_add_f32_e32 v75, v153, v75
	v_pk_add_f32 v[50:51], v[50:51], v[126:127] op_sel_hi:[1,0] neg_lo:[0,1] neg_hi:[0,1]
	v_add_f32_e32 v75, v154, v75
	v_pk_mul_f32 v[156:157], v[50:51], v[50:51]
	v_add_f32_e32 v75, v155, v75
	v_pk_add_f32 v[52:53], v[52:53], v[126:127] op_sel_hi:[1,0] neg_lo:[0,1] neg_hi:[0,1]
	v_add_f32_e32 v75, v156, v75
	v_pk_mul_f32 v[158:159], v[52:53], v[52:53]
	v_add_f32_e32 v75, v157, v75
	v_pk_add_f32 v[54:55], v[54:55], v[126:127] op_sel_hi:[1,0] neg_lo:[0,1] neg_hi:[0,1]
	v_add_f32_e32 v75, v158, v75
	v_pk_mul_f32 v[160:161], v[54:55], v[54:55]
	v_add_f32_e32 v75, v159, v75
	v_pk_add_f32 v[56:57], v[56:57], v[126:127] op_sel_hi:[1,0] neg_lo:[0,1] neg_hi:[0,1]
	v_add_f32_e32 v75, v160, v75
	v_pk_mul_f32 v[126:127], v[56:57], v[56:57]
	v_add_f32_e32 v75, v161, v75
	v_add_f32_e32 v75, v126, v75
	v_add_f32_e32 v75, v127, v75
	s_nop 1
	v_add_f32_dpp v75, v75, v75 quad_perm:[1,0,3,2] row_mask:0xf bank_mask:0xf bound_ctrl:1
	s_nop 1
	v_add_f32_dpp v75, v75, v75 quad_perm:[2,3,0,1] row_mask:0xf bank_mask:0xf bound_ctrl:1
	s_nop 1
	v_add_f32_dpp v75, v75, v75 row_half_mirror row_mask:0xf bank_mask:0xf bound_ctrl:1
	s_nop 1
	v_add_f32_dpp v75, v75, v75 row_mirror row_mask:0xf bank_mask:0xf bound_ctrl:1
	v_mov_b32_e32 v126, v75
	s_nop 1
	v_permlane16_swap_b32_e32 v75, v126
	v_add_f32_e32 v75, v75, v126
	v_mov_b32_e32 v126, v75
	s_nop 1
	v_permlane32_swap_b32_e32 v75, v126
	v_add_f32_e32 v75, v75, v126
	v_fmamk_f32 v75, v75, 0x3a000000, v105
	v_mul_f32_e32 v126, 0x4f800000, v75
	v_cmp_gt_f32_e32 vcc, s23, v75
	s_nop 1
	v_cndmask_b32_e32 v75, v75, v126, vcc
	v_sqrt_f32_e32 v126, v75
	s_nop 0
	v_add_u32_e32 v127, -1, v126
	v_fma_f32 v130, -v127, v126, v75
	v_cmp_ge_f32_e64 s[8:9], 0, v130
	v_add_u32_e32 v130, 1, v126
	s_nop 0
	v_cndmask_b32_e64 v127, v126, v127, s[8:9]
	v_fma_f32 v126, -v130, v126, v75
	v_cmp_lt_f32_e64 s[8:9], 0, v126
	s_nop 1
	v_cndmask_b32_e64 v126, v127, v130, s[8:9]
	v_mul_f32_e32 v127, 0x37800000, v126
	v_cndmask_b32_e32 v126, v126, v127, vcc
	v_cmp_class_f32_e32 vcc, v75, v106
	s_nop 1
	v_cndmask_b32_e32 v75, v126, v75, vcc
	v_div_scale_f32 v126, s[8:9], v75, v75, 1.0
	v_rcp_f32_e32 v127, v126
	s_nop 0
	v_fma_f32 v130, -v126, v127, 1.0
	v_fmac_f32_e32 v127, v130, v127
	v_div_scale_f32 v130, vcc, 1.0, v75, 1.0
	v_mul_f32_e32 v131, v130, v127
	v_fma_f32 v134, -v126, v131, v130
	v_fmac_f32_e32 v131, v134, v127
	v_fma_f32 v126, -v126, v131, v130
	v_div_fmas_f32 v126, v126, v127, v131
	v_div_fixup_f32 v126, v126, v75, 1.0
	v_pk_mul_f32 v[124:125], v[124:125], v[126:127] op_sel_hi:[1,0]
	v_pk_mul_f32 v[112:113], v[112:113], v[126:127] op_sel_hi:[1,0]
	v_pk_mul_f32 v[130:131], v[132:133], v[126:127] op_sel_hi:[1,0]
	v_pk_mul_f32 v[128:129], v[128:129], v[126:127] op_sel_hi:[1,0]
	v_pk_mul_f32 v[54:55], v[54:55], v[126:127] op_sel_hi:[1,0]
	v_pk_mul_f32 v[114:115], v[114:115], v[126:127] op_sel_hi:[1,0]
	v_pk_mul_f32 v[120:121], v[120:121], v[126:127] op_sel_hi:[1,0]
	v_pk_mul_f32 v[116:117], v[116:117], v[126:127] op_sel_hi:[1,0]
	v_pk_mul_f32 v[110:111], v[110:111], v[126:127] op_sel_hi:[1,0]
	v_pk_mul_f32 v[56:57], v[56:57], v[126:127] op_sel_hi:[1,0]
	s_waitcnt lgkmcnt(7)
	v_pk_fma_f32 v[82:83], v[82:83], v[124:125], v[34:35]
	v_pk_fma_f32 v[80:81], v[80:81], v[112:113], v[36:37]
	s_waitcnt lgkmcnt(6)
	v_pk_fma_f32 v[112:113], v[78:79], v[130:131], v[30:31]
	v_pk_fma_f32 v[84:85], v[84:85], v[128:129], v[32:33]
	s_waitcnt lgkmcnt(0)
	v_pk_fma_f32 v[124:125], v[54:55], v[2:3], v[6:7]
	v_pk_add_f32 v[2:3], v[4:5], 0 op_sel_hi:[1,0]
	v_pk_mul_f32 v[58:59], v[58:59], v[126:127] op_sel_hi:[1,0]
	v_pk_mul_f32 v[60:61], v[60:61], v[126:127] op_sel_hi:[1,0]
	v_pk_mul_f32 v[122:123], v[122:123], v[126:127] op_sel_hi:[1,0]
	v_pk_mul_f32 v[118:119], v[118:119], v[126:127] op_sel_hi:[1,0]
	v_pk_mul_f32 v[50:51], v[50:51], v[126:127] op_sel_hi:[1,0]
	v_pk_mul_f32 v[52:53], v[52:53], v[126:127] op_sel_hi:[1,0]
	v_pk_fma_f32 v[90:91], v[90:91], v[114:115], v[26:27]
	v_pk_fma_f32 v[88:89], v[88:89], v[120:121], v[28:29]
	v_pk_fma_f32 v[86:87], v[86:87], v[116:117], v[18:19]
	v_pk_fma_f32 v[92:93], v[92:93], v[110:111], v[20:21]
	v_pk_fma_f32 v[126:127], v[56:57], v[2:3], v[8:9]
	v_cvt_pk_bf16_f32 v2, v82, v83
	v_cvt_pk_bf16_f32 v3, v80, v81
	v_cvt_pk_bf16_f32 v4, v112, v113
	v_cvt_pk_bf16_f32 v5, v84, v85
	v_pk_fma_f32 v[110:111], v[42:43], v[58:59], v[22:23]
	v_pk_fma_f32 v[114:115], v[44:45], v[60:61], v[24:25]
	v_pk_fma_f32 v[116:117], v[46:47], v[122:123], v[14:15]
	v_pk_fma_f32 v[118:119], v[48:49], v[118:119], v[16:17]
	global_store_dwordx4 v[76:77], v[2:5], off
	v_pk_fma_f32 v[120:121], v[50:51], v[38:39], v[10:11]
	v_pk_fma_f32 v[122:123], v[52:53], v[40:41], v[12:13]
	v_cvt_pk_bf16_f32 v2, v90, v91
	v_cvt_pk_bf16_f32 v3, v88, v89
	v_cvt_pk_bf16_f32 v4, v86, v87
	v_cvt_pk_bf16_f32 v5, v92, v93
	global_store_dwordx4 v[76:77], v[2:5], off offset:1024
	s_nop 1
	v_cvt_pk_bf16_f32 v2, v110, v111
	v_cvt_pk_bf16_f32 v3, v114, v115
	v_cvt_pk_bf16_f32 v4, v116, v117
	v_cvt_pk_bf16_f32 v5, v118, v119
	global_store_dwordx4 v[76:77], v[2:5], off offset:2048
	s_nop 1
	v_cvt_pk_bf16_f32 v2, v120, v121
	v_cvt_pk_bf16_f32 v3, v122, v123
	v_cvt_pk_bf16_f32 v4, v124, v125
	v_cvt_pk_bf16_f32 v5, v126, v127
	global_store_dwordx4 v[76:77], v[2:5], off offset:3072
	s_nop 1
; __device__ __forceinline__ float wave_sum(float v) { return xor32_sum(xor16_sum(row16_sum(v))); }
; __device__ __forceinline__ void row_ln(float (&v)[32]) {
;     float s = 0.f;
; #pragma unroll
;     for (int i = 0; i < 32; ++i) s += v[i];
;     const float mean = wave_sum(s) * (1.0f / DM); float q = 0.f;
; #pragma unroll
;     for (int i = 0; i < 32; ++i) { v[i] -= mean; q += v[i] * v[i]; }
;     const float rstd = 1.0f / sqrtf(wave_sum(q) * (1.0f / DM) + LN_EPS);
; #pragma unroll
;     for (int i = 0; i < 32; ++i) v[i] *= rstd;
; }
; __device__ __forceinline__ void ph_post1(Ctx& C, int l, int nrows, bool dry = false) {
;     ...
;             row_ln(v); row_affine_lds(v, PAR + 6144, PAR + 8192, C.lane, 1.0f);
	v_add_f32_e32 v2, 0, v82
	v_add_f32_e32 v2, v83, v2
	v_add_f32_e32 v2, v80, v2
	v_add_f32_e32 v2, v81, v2
	v_add_f32_e32 v2, v112, v2
	v_add_f32_e32 v2, v113, v2
	v_add_f32_e32 v2, v84, v2
	v_add_f32_e32 v2, v85, v2
	v_add_f32_e32 v2, v90, v2
	v_add_f32_e32 v2, v91, v2
	v_add_f32_e32 v2, v88, v2
	v_add_f32_e32 v2, v89, v2
	v_add_f32_e32 v2, v86, v2
	v_add_f32_e32 v2, v87, v2
	v_add_f32_e32 v2, v92, v2
	v_add_f32_e32 v2, v93, v2
	v_add_f32_e32 v2, v110, v2
	v_add_f32_e32 v2, v111, v2
	v_add_f32_e32 v2, v114, v2
	v_add_f32_e32 v2, v115, v2
	v_add_f32_e32 v2, v116, v2
	v_add_f32_e32 v2, v117, v2
	v_add_f32_e32 v2, v118, v2
	v_add_f32_e32 v2, v119, v2
	v_add_f32_e32 v2, v120, v2
	v_add_f32_e32 v2, v121, v2
	v_add_f32_e32 v2, v122, v2
	v_add_f32_e32 v2, v123, v2
	v_add_f32_e32 v2, v124, v2
	v_add_f32_e32 v2, v125, v2
	v_add_f32_e32 v2, v126, v2
	v_add_f32_e32 v2, v127, v2
	s_nop 1
	v_add_f32_dpp v2, v2, v2 quad_perm:[1,0,3,2] row_mask:0xf bank_mask:0xf bound_ctrl:1
	s_nop 1
	v_add_f32_dpp v2, v2, v2 quad_perm:[2,3,0,1] row_mask:0xf bank_mask:0xf bound_ctrl:1
	s_nop 1
	v_add_f32_dpp v2, v2, v2 row_half_mirror row_mask:0xf bank_mask:0xf bound_ctrl:1
	s_nop 1
	v_add_f32_dpp v2, v2, v2 row_mirror row_mask:0xf bank_mask:0xf bound_ctrl:1
	v_mov_b32_e32 v3, v2
	s_nop 1
	v_permlane16_swap_b32_e32 v2, v3
	v_add_f32_e32 v2, v2, v3
	v_mov_b32_e32 v3, v2
	s_nop 1
	v_permlane32_swap_b32_e32 v2, v3
	v_add_f32_e32 v2, v2, v3
	v_mul_f32_e32 v128, 0x3a000000, v2
	v_pk_add_f32 v[82:83], v[82:83], v[128:129] op_sel_hi:[1,0] neg_lo:[0,1] neg_hi:[0,1]
	v_pk_add_f32 v[80:81], v[80:81], v[128:129] op_sel_hi:[1,0] neg_lo:[0,1] neg_hi:[0,1]
	v_pk_mul_f32 v[130:131], v[82:83], v[82:83]
	v_pk_mul_f32 v[132:133], v[80:81], v[80:81]
	v_add_f32_e32 v75, v130, v131
	v_pk_add_f32 v[112:113], v[112:113], v[128:129] op_sel_hi:[1,0] neg_lo:[0,1] neg_hi:[0,1]
	v_add_f32_e32 v75, v132, v75
	v_pk_mul_f32 v[134:135], v[112:113], v[112:113]
	v_add_f32_e32 v75, v133, v75
	v_pk_add_f32 v[84:85], v[84:85], v[128:129] op_sel_hi:[1,0] neg_lo:[0,1] neg_hi:[0,1]
	v_add_f32_e32 v75, v134, v75
	v_pk_mul_f32 v[136:137], v[84:85], v[84:85]
	v_add_f32_e32 v75, v135, v75
	v_pk_add_f32 v[90:91], v[90:91], v[128:129] op_sel_hi:[1,0] neg_lo:[0,1] neg_hi:[0,1]
	v_add_f32_e32 v75, v136, v75
	v_pk_mul_f32 v[138:139], v[90:91], v[90:91]
	v_add_f32_e32 v75, v137, v75
	v_pk_add_f32 v[88:89], v[88:89], v[128:129] op_sel_hi:[1,0] neg_lo:[0,1] neg_hi:[0,1]
	v_add_f32_e32 v75, v138, v75
	v_pk_mul_f32 v[140:141], v[88:89], v[88:89]
	v_add_f32_e32 v75, v139, v75
	v_pk_add_f32 v[86:87], v[86:87], v[128:129] op_sel_hi:[1,0] neg_lo:[0,1] neg_hi:[0,1]
	v_add_f32_e32 v75, v140, v75
	v_pk_mul_f32 v[142:143], v[86:87], v[86:87]
	v_add_f32_e32 v75, v141, v75
	v_pk_add_f32 v[92:93], v[92:93], v[128:129] op_sel_hi:[1,0] neg_lo:[0,1] neg_hi:[0,1]
	v_add_f32_e32 v75, v142, v75
	v_pk_mul_f32 v[144:145], v[92:93], v[92:93]
	v_add_f32_e32 v75, v143, v75
	v_pk_add_f32 v[110:111], v[110:111], v[128:129] op_sel_hi:[1,0] neg_lo:[0,1] neg_hi:[0,1]
	v_add_f32_e32 v75, v144, v75
	v_pk_mul_f32 v[146:147], v[110:111], v[110:111]
	v_add_f32_e32 v75, v145, v75
	v_pk_add_f32 v[114:115], v[114:115], v[128:129] op_sel_hi:[1,0] neg_lo:[0,1] neg_hi:[0,1]
	v_add_f32_e32 v75, v146, v75
	v_pk_mul_f32 v[148:149], v[114:115], v[114:115]
	v_add_f32_e32 v75, v147, v75
	v_pk_add_f32 v[116:117], v[116:117], v[128:129] op_sel_hi:[1,0] neg_lo:[0,1] neg_hi:[0,1]
	v_add_f32_e32 v75, v148, v75
	v_pk_mul_f32 v[150:151], v[116:117], v[116:117]
	v_add_f32_e32 v75, v149, v75
	v_pk_add_f32 v[118:119], v[118:119], v[128:129] op_sel_hi:[1,0] neg_lo:[0,1] neg_hi:[0,1]
	v_add_f32_e32 v75, v150, v75
	v_pk_mul_f32 v[152:153], v[118:119], v[118:119]
	v_add_f32_e32 v75, v151, v75
	v_pk_add_f32 v[120:121], v[120:121], v[128:129] op_sel_hi:[1,0] neg_lo:[0,1] neg_hi:[0,1]
	v_add_f32_e32 v75, v152, v75
	v_pk_mul_f32 v[154:155], v[120:121], v[120:121]
	v_add_f32_e32 v75, v153, v75
	v_pk_add_f32 v[122:123], v[122:123], v[128:129] op_sel_hi:[1,0] neg_lo:[0,1] neg_hi:[0,1]
	v_add_f32_e32 v75, v154, v75
	v_pk_mul_f32 v[156:157], v[122:123], v[122:123]
	v_add_f32_e32 v75, v155, v75
	v_pk_add_f32 v[124:125], v[124:125], v[128:129] op_sel_hi:[1,0] neg_lo:[0,1] neg_hi:[0,1]
	v_add_f32_e32 v75, v156, v75
	v_pk_mul_f32 v[158:159], v[124:125], v[124:125]
	v_add_f32_e32 v75, v157, v75
	v_pk_add_f32 v[126:127], v[126:127], v[128:129] op_sel_hi:[1,0] neg_lo:[0,1] neg_hi:[0,1]
	v_add_f32_e32 v75, v158, v75
	v_pk_mul_f32 v[128:129], v[126:127], v[126:127]
	v_add_f32_e32 v75, v159, v75
	v_add_f32_e32 v75, v128, v75
	v_add_f32_e32 v75, v129, v75
	ds_read_b128 v[2:5], v107
	ds_read_b128 v[6:9], v107 offset:16
	ds_read_b128 v[10:13], v107 offset:2048
	ds_read_b128 v[14:17], v107 offset:2064
	ds_read_b128 v[18:21], v107 offset:4096
	ds_read_b128 v[22:25], v107 offset:4112
	ds_read_b128 v[26:29], v107 offset:6144
	ds_read_b128 v[30:33], v107 offset:6160
	ds_read_b128 v[34:37], v108
	ds_read_b128 v[38:41], v108 offset:16
	ds_read_b128 v[42:45], v108 offset:2048
	ds_read_b128 v[46:49], v108 offset:2064
	ds_read_b128 v[50:53], v108 offset:4096
	ds_read_b128 v[54:57], v108 offset:4112
	ds_read_b128 v[58:61], v108 offset:6144
	ds_read_b128 v[76:79], v108 offset:6160
	v_add_f32_dpp v75, v75, v75 quad_perm:[1,0,3,2] row_mask:0xf bank_mask:0xf bound_ctrl:1
	s_waitcnt lgkmcnt(14)
	v_pk_add_f32 v[2:3], v[2:3], 1.0 op_sel_hi:[1,0]
	v_pk_add_f32 v[4:5], v[4:5], 1.0 op_sel_hi:[1,0]
	v_add_f32_dpp v75, v75, v75 quad_perm:[2,3,0,1] row_mask:0xf bank_mask:0xf bound_ctrl:1
	v_pk_add_f32 v[6:7], v[6:7], 1.0 op_sel_hi:[1,0]
	s_waitcnt lgkmcnt(13)
; #define LAS __attribute__((address_space(3)))
; __device__ __forceinline__ void ph_post1(Ctx& C, int l, int nrows, bool dry = false) {
;     ...
;             row_ln(v); row_affine_lds(v, PAR + 6144, PAR + 8192, C.lane, 1.0f);
;             row_store_fp8(WSP(unsigned char, WS_HB8) + (size_t)row * DM, C.lane, v);
; #pragma unroll
;             for (int j = 0; j < 4; ++j) { *(LAS f32x4*)(H2 + C.wave * DM + 512 * j + 8 * C.lane) = (f32x4){v[8 * j], v[8 * j + 1], v[8 * j + 2], v[8 * j + 3]};
;                 *(LAS f32x4*)(H2 + C.wave * DM + 512 * j + 8 * C.lane + 4) = (f32x4){v[8 * j + 4], v[8 * j + 5], v[8 * j + 6], v[8 * j + 7]}; }
;         }
;         __syncthreads();
;         {
;             const int e4 = C.lane & 7, cg = C.lane >> 3, cbase = 256 * C.wave + 32 * cg;
;             f32x2 acc[8][2];
; #pragma unroll
;             for (int r = 0; r < 8; ++r) { acc[r][0] = (f32x2){0.f, 0.f}; acc[r][1] = (f32x2){0.f, 0.f}; }
	v_pk_add_f32 v[10:11], v[10:11], 1.0 op_sel_hi:[1,0]
	v_add_f32_dpp v75, v75, v75 row_half_mirror row_mask:0xf bank_mask:0xf bound_ctrl:1
	s_waitcnt lgkmcnt(12)
	v_pk_add_f32 v[14:15], v[14:15], 1.0 op_sel_hi:[1,0]
	v_pk_add_f32 v[8:9], v[8:9], 1.0 op_sel_hi:[1,0]
	v_add_f32_dpp v75, v75, v75 row_mirror row_mask:0xf bank_mask:0xf bound_ctrl:1
	v_mov_b32_e32 v128, v75
	s_nop 1
	v_permlane16_swap_b32_e32 v75, v128
	v_add_f32_e32 v75, v75, v128
	v_mov_b32_e32 v128, v75
	s_nop 1
	v_permlane32_swap_b32_e32 v75, v128
	v_add_f32_e32 v75, v75, v128
	v_fmamk_f32 v75, v75, 0x3a000000, v105
	v_mul_f32_e32 v128, 0x4f800000, v75
	v_cmp_gt_f32_e32 vcc, s23, v75
	s_waitcnt lgkmcnt(11)
	v_pk_add_f32 v[18:19], v[18:19], 1.0 op_sel_hi:[1,0]
	s_waitcnt lgkmcnt(10)
	v_pk_add_f32 v[22:23], v[22:23], 1.0 op_sel_hi:[1,0]
	v_cndmask_b32_e32 v75, v75, v128, vcc
	v_sqrt_f32_e32 v128, v75
	s_waitcnt lgkmcnt(9)
	v_pk_add_f32 v[26:27], v[26:27], 1.0 op_sel_hi:[1,0]
	s_waitcnt lgkmcnt(8)
	v_pk_add_f32 v[30:31], v[30:31], 1.0 op_sel_hi:[1,0]
	v_pk_add_f32 v[12:13], v[12:13], 1.0 op_sel_hi:[1,0]
	v_add_u32_e32 v129, -1, v128
	v_fma_f32 v130, -v129, v128, v75
	v_cmp_ge_f32_e64 s[8:9], 0, v130
	v_add_u32_e32 v130, 1, v128
	v_pk_add_f32 v[16:17], v[16:17], 1.0 op_sel_hi:[1,0]
	v_cndmask_b32_e64 v129, v128, v129, s[8:9]
	v_fma_f32 v128, -v130, v128, v75
	v_cmp_lt_f32_e64 s[8:9], 0, v128
	v_pk_add_f32 v[20:21], v[20:21], 1.0 op_sel_hi:[1,0]
	v_pk_add_f32 v[24:25], v[24:25], 1.0 op_sel_hi:[1,0]
	v_cndmask_b32_e64 v128, v129, v130, s[8:9]
	v_mul_f32_e32 v129, 0x37800000, v128
	v_cndmask_b32_e32 v128, v128, v129, vcc
	v_cmp_class_f32_e32 vcc, v75, v106
	v_pk_add_f32 v[28:29], v[28:29], 1.0 op_sel_hi:[1,0]
	v_pk_add_f32 v[32:33], v[32:33], 1.0 op_sel_hi:[1,0]
	v_cndmask_b32_e32 v75, v128, v75, vcc
	v_div_scale_f32 v128, s[8:9], v75, v75, 1.0
	v_rcp_f32_e32 v129, v128
	s_mov_b32 s8, -4
	v_fma_f32 v130, -v128, v129, 1.0
	v_fmac_f32_e32 v129, v130, v129
	v_div_scale_f32 v130, vcc, 1.0, v75, 1.0
	v_mul_f32_e32 v131, v130, v129
	v_fma_f32 v132, -v128, v131, v130
	v_fmac_f32_e32 v131, v132, v129
	v_fma_f32 v128, -v128, v131, v130
	v_div_fmas_f32 v128, v128, v129, v131
	v_div_fixup_f32 v128, v128, v75, 1.0
	v_pk_mul_f32 v[82:83], v[82:83], v[128:129] op_sel_hi:[1,0]
	v_pk_mul_f32 v[80:81], v[80:81], v[128:129] op_sel_hi:[1,0]
	v_pk_mul_f32 v[112:113], v[112:113], v[128:129] op_sel_hi:[1,0]
	v_pk_mul_f32 v[90:91], v[90:91], v[128:129] op_sel_hi:[1,0]
	v_pk_mul_f32 v[86:87], v[86:87], v[128:129] op_sel_hi:[1,0]
	s_waitcnt lgkmcnt(7)
	v_pk_fma_f32 v[2:3], v[2:3], v[82:83], v[34:35]
	v_pk_fma_f32 v[4:5], v[4:5], v[80:81], v[36:37]
	s_waitcnt lgkmcnt(6)
	v_pk_fma_f32 v[6:7], v[6:7], v[112:113], v[38:39]
	v_mov_b32_e32 v36, 0
	v_mov_b32_e32 v37, 0
	v_pk_mul_f32 v[84:85], v[84:85], v[128:129] op_sel_hi:[1,0]
	v_pk_mul_f32 v[110:111], v[110:111], v[128:129] op_sel_hi:[1,0]
	v_pk_mul_f32 v[116:117], v[116:117], v[128:129] op_sel_hi:[1,0]
	s_waitcnt lgkmcnt(5)
	v_pk_fma_f32 v[10:11], v[10:11], v[90:91], v[42:43]
	s_waitcnt lgkmcnt(4)
	v_pk_fma_f32 v[14:15], v[14:15], v[86:87], v[46:47]
	v_cvt_pk_fp8_f32 v36, v2, v3
	v_cvt_pk_fp8_f32 v37, v6, v7
	v_mov_b32_e32 v38, 0
	v_mov_b32_e32 v39, 0
	v_pk_mul_f32 v[120:121], v[120:121], v[128:129] op_sel_hi:[1,0]
	v_pk_mul_f32 v[124:125], v[124:125], v[128:129] op_sel_hi:[1,0]
	v_pk_fma_f32 v[8:9], v[8:9], v[84:85], v[40:41]
	s_waitcnt lgkmcnt(3)
	v_pk_fma_f32 v[18:19], v[18:19], v[110:111], v[50:51]
	s_waitcnt lgkmcnt(2)
	v_pk_fma_f32 v[22:23], v[116:117], v[22:23], v[54:55]
	v_cvt_pk_fp8_f32 v38, v10, v11
	v_cvt_pk_fp8_f32 v39, v14, v15
	v_mov_b32_e32 v40, 0
	v_mov_b32_e32 v41, 0
	s_waitcnt lgkmcnt(1)
	v_pk_fma_f32 v[26:27], v[120:121], v[26:27], v[58:59]
	s_waitcnt lgkmcnt(0)
	v_pk_fma_f32 v[30:31], v[124:125], v[30:31], v[76:77]
	v_cvt_pk_fp8_f32 v40, v18, v19
	v_cvt_pk_fp8_f32 v41, v22, v23
	v_mov_b32_e32 v42, 0
	v_mov_b32_e32 v43, 0
	v_pk_mul_f32 v[88:89], v[88:89], v[128:129] op_sel_hi:[1,0]
	v_pk_mul_f32 v[92:93], v[92:93], v[128:129] op_sel_hi:[1,0]
	v_cvt_pk_fp8_f32 v42, v26, v27
	v_cvt_pk_fp8_f32 v43, v30, v31
	v_pk_mul_f32 v[114:115], v[114:115], v[128:129] op_sel_hi:[1,0]
	v_pk_mul_f32 v[118:119], v[118:119], v[128:129] op_sel_hi:[1,0]
	v_pk_fma_f32 v[12:13], v[12:13], v[88:89], v[44:45]
	v_pk_fma_f32 v[16:17], v[16:17], v[92:93], v[48:49]
	v_cvt_pk_fp8_f32 v36, v4, v5 op_sel:[0,0,1]
	v_cvt_pk_fp8_f32 v37, v8, v9 op_sel:[0,0,1]
	v_pk_mul_f32 v[122:123], v[122:123], v[128:129] op_sel_hi:[1,0]
	v_pk_mul_f32 v[126:127], v[126:127], v[128:129] op_sel_hi:[1,0]
	v_pk_fma_f32 v[20:21], v[20:21], v[114:115], v[52:53]
	v_pk_fma_f32 v[24:25], v[118:119], v[24:25], v[56:57]
	v_cvt_pk_fp8_f32 v38, v12, v13 op_sel:[0,0,1]
	v_cvt_pk_fp8_f32 v39, v16, v17 op_sel:[0,0,1]
	v_pk_fma_f32 v[28:29], v[122:123], v[28:29], v[60:61]
	v_pk_fma_f32 v[32:33], v[126:127], v[32:33], v[78:79]
	v_cvt_pk_fp8_f32 v40, v20, v21 op_sel:[0,0,1]
	v_cvt_pk_fp8_f32 v41, v24, v25 op_sel:[0,0,1]
	v_lshl_add_u64 v[34:35], v[68:69], 0, s[26:27]
	v_cvt_pk_fp8_f32 v42, v28, v29 op_sel:[0,0,1]
	v_cvt_pk_fp8_f32 v43, v32, v33 op_sel:[0,0,1]
	global_store_dwordx2 v[34:35], v[36:37], off
	global_store_dwordx2 v[34:35], v[38:39], off offset:512
	global_store_dwordx2 v[34:35], v[40:41], off offset:1024
	global_store_dwordx2 v[34:35], v[42:43], off offset:1536
	v_add_u32_e32 v34, s15, v1
	v_mov_b32_e32 v84, v101
	v_mov_b64_e32 v[58:59], v[70:71]
	v_mov_b32_e32 v75, v74
	v_mov_b32_e32 v38, v74
	v_mov_b32_e32 v39, v74
	v_mov_b32_e32 v40, v74
	v_mov_b32_e32 v41, v74
	v_mov_b32_e32 v42, v74
	v_mov_b32_e32 v43, v74
	v_mov_b32_e32 v44, v74
	v_mov_b32_e32 v45, v74
	v_mov_b32_e32 v46, v74
	v_mov_b32_e32 v47, v74
	v_mov_b32_e32 v48, v74
	v_mov_b32_e32 v49, v74
	v_mov_b32_e32 v50, v74
	v_mov_b32_e32 v51, v74
	v_mov_b32_e32 v52, v74
	v_mov_b32_e32 v53, v74
	v_mov_b32_e32 v54, v74
	v_mov_b32_e32 v55, v74
	v_mov_b32_e32 v56, v74
	v_mov_b32_e32 v57, v74
	v_mov_b32_e32 v60, v74
	v_mov_b32_e32 v61, v74
	v_mov_b32_e32 v76, v74
	v_mov_b32_e32 v77, v74
	v_mov_b32_e32 v78, v74
	v_mov_b32_e32 v79, v74
	v_mov_b32_e32 v80, v74
	v_mov_b32_e32 v81, v74
	v_mov_b32_e32 v82, v74
	v_mov_b32_e32 v83, v74
	ds_write_b128 v34, v[2:5]
	ds_write_b128 v34, v[6:9] offset:16
	ds_write_b128 v34, v[10:13] offset:2048
	ds_write_b128 v34, v[14:17] offset:2064
	ds_write_b128 v34, v[18:21] offset:4096
	ds_write_b128 v34, v[22:25] offset:4112
	ds_write_b128 v34, v[26:29] offset:6144
	ds_write_b128 v34, v[30:33] offset:6160
	s_waitcnt lgkmcnt(0)
	s_barrier

; __global__ void __launch_bounds__(512, 2) fwd_kernel(Args args) {
	.amdhsa_kernel _Z10fwd_kernel4Args
		.amdhsa_group_segment_fixed_size 0
		.amdhsa_private_segment_fixed_size 0
		.amdhsa_kernarg_size 560
		.amdhsa_user_sgpr_count 2
		.amdhsa_user_sgpr_dispatch_ptr 0
		.amdhsa_user_sgpr_queue_ptr 0
		.amdhsa_user_sgpr_kernarg_segment_ptr 1
		.amdhsa_user_sgpr_dispatch_id 0
		.amdhsa_user_sgpr_kernarg_preload_length 0
		.amdhsa_user_sgpr_kernarg_preload_offset 0
		.amdhsa_user_sgpr_private_segment_size 0
		.amdhsa_uses_dynamic_stack 0
		.amdhsa_enable_private_segment 0
		.amdhsa_system_sgpr_workgroup_id_x 1
		.amdhsa_system_sgpr_workgroup_id_y 0
		.amdhsa_system_sgpr_workgroup_id_z 0
		.amdhsa_system_sgpr_workgroup_info 0
		.amdhsa_system_vgpr_workitem_id 0
		.amdhsa_next_free_vgpr 248
		.amdhsa_next_free_sgpr 98
		.amdhsa_accum_offset 248
		.amdhsa_reserve_vcc 1
		.amdhsa_float_round_mode_32 0
		.amdhsa_float_round_mode_16_64 0
		.amdhsa_float_denorm_mode_32 3
		.amdhsa_float_denorm_mode_16_64 3
		.amdhsa_dx10_clamp 1
		.amdhsa_ieee_mode 1
		.amdhsa_fp16_overflow 0
		.amdhsa_tg_split 0
		.amdhsa_exception_fp_ieee_invalid_op 0
		.amdhsa_exception_fp_denorm_src 0
		.amdhsa_exception_fp_ieee_div_zero 0
		.amdhsa_exception_fp_ieee_overflow 0
		.amdhsa_exception_fp_ieee_underflow 0
		.amdhsa_exception_fp_ieee_inexact 0
		.amdhsa_exception_int_div_zero 0
	.end_amdhsa_kernel

; __global__ void __launch_bounds__(512, 2) fwd_kernel(Args args) {
amdhsa.kernels:
  - .agpr_count:     0
    .args:
      - .offset:         0
        .size:           304
        .value_kind:     by_value
      - .offset:         304
        .size:           4
        .value_kind:     hidden_block_count_x
      - .offset:         308
        .size:           4
        .value_kind:     hidden_block_count_y
      - .offset:         312
        .size:           4
        .value_kind:     hidden_block_count_z
      - .offset:         316
        .size:           2
        .value_kind:     hidden_group_size_x
      - .offset:         318
        .size:           2
        .value_kind:     hidden_group_size_y
      - .offset:         320
        .size:           2
        .value_kind:     hidden_group_size_z
      - .offset:         322
        .size:           2
        .value_kind:     hidden_remainder_x
      - .offset:         324
        .size:           2
        .value_kind:     hidden_remainder_y
      - .offset:         326
        .size:           2
        .value_kind:     hidden_remainder_z
      - .offset:         344
        .size:           8
        .value_kind:     hidden_global_offset_x
      - .offset:         352
        .size:           8
        .value_kind:     hidden_global_offset_y
      - .offset:         360
        .size:           8
        .value_kind:     hidden_global_offset_z
      - .offset:         368
        .size:           2
        .value_kind:     hidden_grid_dims
      - .offset:         424
        .size:           4
        .value_kind:     hidden_dynamic_lds_size
    .group_segment_fixed_size: 0
    .kernarg_segment_align: 8
    .kernarg_segment_size: 560
    .language:       OpenCL C
    .language_version:
      - 2
      - 0
    .max_flat_workgroup_size: 512
    .name:           _Z10fwd_kernel4Args
    .private_segment_fixed_size: 0
    .sgpr_count:     104
    .sgpr_spill_count: 12
    .symbol:         _Z10fwd_kernel4Args.kd
    .uniform_work_group_size: 1
    .uses_dynamic_stack: false
    .vgpr_count:     248
    .vgpr_spill_count: 0
    .wavefront_size: 64
